# P1 norm0 loop software-pipelined (all loads in flight, next row prefetched); MLA attention LDS ring deepened to 3 slots with counted vmcnt
# speedup vs baseline: 1.0400x; 1.0091x over previous
; DI void norm_mod_store(const f32x4 (&v)[8], const float* gain, const float* shift, const float* scale, bf16_t* hrow, int lane, unsigned char* h8row = nullptr) {
;     float ss = 0.f;
; #pragma unroll
;     for (int i = 0; i < 8; ++i) ss += v[i][0] * v[i][0] + v[i][1] * v[i][1] + v[i][2] * v[i][2] + v[i][3] * v[i][3];
;     ss = wave_sum(ss);
;     const float r = rsqrtf(ss * (1.0f / DM) + EPS);
; DI void phase_norm0(const Params& p, int G, int bid) {
;     const int lane = threadIdx.x & 63, wave = threadIdx.x >> 6;
;     const float* MOD = (const float*)(p.ws + WS_MOD);
;     bf16_t* H = (bf16_t*)(p.ws + WS_H);
;     for (int row = bid * 8 + wave; row < NTOK; row += G * 8) {
;         const float* xr = row < NCTX ? p.in[2] + (size_t)row * DM : p.in[0] + (size_t)(row - NCTX) * DM;
;         f32x4 v[8];
; #pragma unroll
;         for (int i = 0; i < 8; ++i) v[i] = *(const f32x4*)(xr + 4 * lane + 256 * i);
;         const float* md = MOD + (size_t)row_mod(row) * MODN;
;         norm_mod_store(v, p.in[9], md, md + DM, H + (size_t)row * DM, lane);
;     }
.LBB0_157:
	s_cmp_gt_i32 s24, 1
	s_cselect_b64 s[0:1], -1, 0
	s_cmp_lt_i32 s25, 2
	s_cselect_b64 s[2:3], -1, 0
	s_or_b64 s[0:1], s[0:1], s[2:3]
	s_and_b64 vcc, exec, s[0:1]
	v_lshrrev_b32_e32 v222, 6, v0
	s_cbranch_vccnz .LBB0_215
	s_mov_b64 s[0:1], exec
	v_readlane_b32 s10, v251, 18
	v_readlane_b32 s11, v251, 19
	v_readfirstlane_b32 s12, v0
	v_and_b32_e32 v82, 63, v0
	v_lshlrev_b32_e32 v1, 4, v82
	v_lshlrev_b32_e32 v35, 3, v82
	v_add_u32_e32 v34, 0x1000, v1
	v_xor_b32_e32 v72, 32, v82
	v_xor_b32_e32 v73, 16, v82
	v_xor_b32_e32 v74, 8, v82
	v_xor_b32_e32 v75, 4, v82
	v_xor_b32_e32 v76, 2, v82
	v_xor_b32_e32 v77, 1, v82
	v_lshlrev_b32_e32 v72, 2, v72
	v_lshlrev_b32_e32 v73, 2, v73
	v_lshlrev_b32_e32 v74, 2, v74
	v_lshlrev_b32_e32 v75, 2, v75
	v_lshlrev_b32_e32 v76, 2, v76
	v_lshlrev_b32_e32 v77, 2, v77
	s_lshr_b32 s12, s12, 6
	s_lshl_b32 s13, s22, 3
	s_add_i32 s13, s13, s12
	global_load_dwordx4 v[110:113], v1, s[10:11] offset:0
	global_load_dwordx4 v[114:117], v1, s[10:11] offset:1024
	global_load_dwordx4 v[118:121], v1, s[10:11] offset:2048
	global_load_dwordx4 v[122:125], v1, s[10:11] offset:3072
	global_load_dwordx4 v[126:129], v34, s[10:11] offset:0
	global_load_dwordx4 v[130:133], v34, s[10:11] offset:1024
	global_load_dwordx4 v[134:137], v34, s[10:11] offset:2048
	global_load_dwordx4 v[138:141], v34, s[10:11] offset:3072
	s_sub_i32 s15, s13, 0x400
	s_cmp_lt_u32 s13, 0x400
	s_cselect_b32 s15, s13, s15
	s_cselect_b32 s2, s56, s52
	s_cselect_b32 s3, s57, s53
	s_lshl_b32 s15, s15, 13
	s_add_u32 s2, s2, s15
	s_addc_u32 s3, s3, 0
	global_load_dwordx4 v[40:43], v1, s[2:3] offset:0 nt
	global_load_dwordx4 v[44:47], v1, s[2:3] offset:1024 nt
	global_load_dwordx4 v[48:51], v1, s[2:3] offset:2048 nt
	global_load_dwordx4 v[52:55], v1, s[2:3] offset:3072 nt
	global_load_dwordx4 v[56:59], v34, s[2:3] offset:0 nt
	global_load_dwordx4 v[60:63], v34, s[2:3] offset:1024 nt
	global_load_dwordx4 v[64:67], v34, s[2:3] offset:2048 nt
	global_load_dwordx4 v[68:71], v34, s[2:3] offset:3072 nt
	s_sub_i32 s15, s13, 0x400
	s_lshr_b32 s15, s15, 11
	s_cmp_lt_u32 s13, 0x400
	s_cselect_b32 s15, 4, s15
	s_mul_i32 s15, s15, 0xc000
	s_add_u32 s4, s50, s15
	s_addc_u32 s5, s51, 0
	s_add_u32 s4, s4, 0x10000
	s_addc_u32 s5, s5, 0
	s_add_u32 s6, s4, 0x2000
	s_addc_u32 s7, s5, 0
	s_lshl_b32 s15, s13, 12
	s_add_u32 s8, s50, s15
	s_addc_u32 s9, s51, 0
	s_add_u32 s8, s8, 0x2420e000
	s_addc_u32 s9, s9, 0
	global_load_dwordx4 v[142:145], v1, s[4:5] offset:0
	global_load_dwordx4 v[174:177], v1, s[6:7] offset:0
	global_load_dwordx4 v[146:149], v1, s[4:5] offset:1024
	global_load_dwordx4 v[178:181], v1, s[6:7] offset:1024
	global_load_dwordx4 v[150:153], v1, s[4:5] offset:2048
	global_load_dwordx4 v[182:185], v1, s[6:7] offset:2048
	global_load_dwordx4 v[154:157], v1, s[4:5] offset:3072
	global_load_dwordx4 v[186:189], v1, s[6:7] offset:3072
	global_load_dwordx4 v[158:161], v34, s[4:5] offset:0
	global_load_dwordx4 v[190:193], v34, s[6:7] offset:0
	global_load_dwordx4 v[162:165], v34, s[4:5] offset:1024
	global_load_dwordx4 v[194:197], v34, s[6:7] offset:1024
	global_load_dwordx4 v[166:169], v34, s[4:5] offset:2048
	global_load_dwordx4 v[198:201], v34, s[6:7] offset:2048
	global_load_dwordx4 v[170:173], v34, s[4:5] offset:3072
	global_load_dwordx4 v[202:205], v34, s[6:7] offset:3072
	s_add_i32 s16, s13, 0x800
	s_cmp_ge_u32 s16, 0x2400
	s_cselect_b32 s16, s13, s16
	s_sub_i32 s15, s16, 0x400
	s_cmp_lt_u32 s16, 0x400
	s_cselect_b32 s15, s16, s15
	s_cselect_b32 s2, s56, s52
	s_cselect_b32 s3, s57, s53
	s_lshl_b32 s15, s15, 13
	s_add_u32 s2, s2, s15
	s_addc_u32 s3, s3, 0
	global_load_dwordx4 v[2:5], v1, s[2:3] offset:0 nt
	global_load_dwordx4 v[6:9], v1, s[2:3] offset:1024 nt
	global_load_dwordx4 v[10:13], v1, s[2:3] offset:2048 nt
	global_load_dwordx4 v[14:17], v1, s[2:3] offset:3072 nt
	global_load_dwordx4 v[18:21], v34, s[2:3] offset:0 nt
	global_load_dwordx4 v[22:25], v34, s[2:3] offset:1024 nt
	global_load_dwordx4 v[26:29], v34, s[2:3] offset:2048 nt
	global_load_dwordx4 v[30:33], v34, s[2:3] offset:3072 nt
	s_waitcnt vmcnt(24)
	v_mul_f32_e32 v80, v41, v41
	v_fmac_f32_e32 v80, v40, v40
	v_fmac_f32_e32 v80, v42, v42
	v_fmac_f32_e32 v80, v43, v43
	v_mul_f32_e32 v82, v45, v45
	v_fmac_f32_e32 v82, v44, v44
	v_fmac_f32_e32 v82, v46, v46
	v_fmac_f32_e32 v82, v47, v47
	v_add_f32_e32 v80, v80, v82
	v_mul_f32_e32 v82, v49, v49
	v_fmac_f32_e32 v82, v48, v48
	v_fmac_f32_e32 v82, v50, v50
	v_fmac_f32_e32 v82, v51, v51
	v_add_f32_e32 v80, v80, v82
	v_mul_f32_e32 v82, v53, v53
	v_fmac_f32_e32 v82, v52, v52
	v_fmac_f32_e32 v82, v54, v54
	v_fmac_f32_e32 v82, v55, v55
	v_add_f32_e32 v80, v80, v82
	v_mul_f32_e32 v82, v57, v57
	v_fmac_f32_e32 v82, v56, v56
	v_fmac_f32_e32 v82, v58, v58
	v_fmac_f32_e32 v82, v59, v59
	v_add_f32_e32 v80, v80, v82
	v_mul_f32_e32 v82, v61, v61
	v_fmac_f32_e32 v82, v60, v60
	v_fmac_f32_e32 v82, v62, v62
	v_fmac_f32_e32 v82, v63, v63
	v_add_f32_e32 v80, v80, v82
	v_mul_f32_e32 v82, v65, v65
	v_fmac_f32_e32 v82, v64, v64
	v_fmac_f32_e32 v82, v66, v66
	v_fmac_f32_e32 v82, v67, v67
	v_add_f32_e32 v80, v80, v82
	v_mul_f32_e32 v82, v69, v69
	v_fmac_f32_e32 v82, v68, v68
	v_fmac_f32_e32 v82, v70, v70
	v_fmac_f32_e32 v82, v71, v71
	v_add_f32_e32 v80, v80, v82
	ds_bpermute_b32 v82, v72, v80
	s_waitcnt lgkmcnt(0)
	v_add_f32_e32 v80, v80, v82
	ds_bpermute_b32 v82, v73, v80
	s_waitcnt lgkmcnt(0)
	v_add_f32_e32 v80, v80, v82
	ds_bpermute_b32 v82, v74, v80
	s_waitcnt lgkmcnt(0)
	v_add_f32_e32 v80, v80, v82
	ds_bpermute_b32 v82, v75, v80
	s_waitcnt lgkmcnt(0)
	v_add_f32_e32 v80, v80, v82
	ds_bpermute_b32 v82, v76, v80
	s_waitcnt lgkmcnt(0)
	v_add_f32_e32 v80, v80, v82
	ds_bpermute_b32 v82, v77, v80
	s_waitcnt lgkmcnt(0)
; DI unsigned pk_bf16(float lo, float hi) { f32x2 v = {lo, hi}; hbf16x2 r = __builtin_convertvector(v, hbf16x2); return __builtin_bit_cast(unsigned, r); }
; DI void norm_mod_store(const f32x4 (&v)[8], const float* gain, const float* shift, const float* scale, bf16_t* hrow, int lane, unsigned char* h8row = nullptr) {
;     ...
;     const float r = rsqrtf(ss * (1.0f / DM) + EPS);
; #pragma unroll
;     for (int i = 0; i < 8; ++i) {
;         const int col = 4 * lane + 256 * i;
;         const f32x4 g = *(const f32x4*)(gain + col), sh = *(const f32x4*)(shift + col), sc = *(const f32x4*)(scale + col);
;         const f32x4 h = (v[i] * r * g) * (1.0f + sc) + sh;
;         if (h8row) *(unsigned*)(h8row + col) = pk_fp8x4(h[0], h[1], h[2], h[3]);
;         else { u32x2 w; w.x = pk_bf16(h[0], h[1]); w.y = pk_bf16(h[2], h[3]); *(u32x2*)(hrow + col) = w; }
;     }
	v_add_f32_e32 v80, v80, v82
	v_mov_b32_e32 v83, 0x358637bd
	v_fmamk_f32 v80, v80, 0x3a000000, v83
	v_cmp_gt_f32_e32 vcc, 0x800000, v80
	v_mul_f32_e32 v82, 0x4b800000, v80
	s_nop 1
	v_cndmask_b32_e32 v80, v80, v82, vcc
	v_rsq_f32_e32 v80, v80
	s_nop 0
	v_mul_f32_e32 v82, 0x45800000, v80
	s_nop 0
	v_cndmask_b32_e32 v80, v80, v82, vcc
	s_waitcnt vmcnt(22)
	v_pk_mul_f32 v[40:41], v[40:41], v[80:81] op_sel_hi:[1,0]
	v_pk_mul_f32 v[42:43], v[42:43], v[80:81] op_sel_hi:[1,0]
	v_pk_add_f32 v[174:175], v[174:175], 1.0 op_sel_hi:[1,0]
	v_pk_add_f32 v[176:177], v[176:177], 1.0 op_sel_hi:[1,0]
	v_pk_mul_f32 v[40:41], v[110:111], v[40:41]
	v_pk_mul_f32 v[42:43], v[112:113], v[42:43]
	v_pk_fma_f32 v[40:41], v[174:175], v[40:41], v[142:143]
	v_pk_fma_f32 v[42:43], v[176:177], v[42:43], v[144:145]
	v_cvt_pk_bf16_f32 v84, v40, v41
	v_cvt_pk_bf16_f32 v85, v42, v43
	global_store_dwordx2 v35, v[84:85], s[8:9] offset:0
	s_waitcnt vmcnt(21)
	v_pk_mul_f32 v[44:45], v[44:45], v[80:81] op_sel_hi:[1,0]
	v_pk_mul_f32 v[46:47], v[46:47], v[80:81] op_sel_hi:[1,0]
	v_pk_add_f32 v[178:179], v[178:179], 1.0 op_sel_hi:[1,0]
	v_pk_add_f32 v[180:181], v[180:181], 1.0 op_sel_hi:[1,0]
	v_pk_mul_f32 v[44:45], v[114:115], v[44:45]
	v_pk_mul_f32 v[46:47], v[116:117], v[46:47]
	v_pk_fma_f32 v[44:45], v[178:179], v[44:45], v[146:147]
	v_pk_fma_f32 v[46:47], v[180:181], v[46:47], v[148:149]
	v_cvt_pk_bf16_f32 v86, v44, v45
	v_cvt_pk_bf16_f32 v87, v46, v47
	global_store_dwordx2 v35, v[86:87], s[8:9] offset:512
	s_waitcnt vmcnt(20)
	v_pk_mul_f32 v[48:49], v[48:49], v[80:81] op_sel_hi:[1,0]
	v_pk_mul_f32 v[50:51], v[50:51], v[80:81] op_sel_hi:[1,0]
	v_pk_add_f32 v[182:183], v[182:183], 1.0 op_sel_hi:[1,0]
	v_pk_add_f32 v[184:185], v[184:185], 1.0 op_sel_hi:[1,0]
	v_pk_mul_f32 v[48:49], v[118:119], v[48:49]
	v_pk_mul_f32 v[50:51], v[120:121], v[50:51]
	v_pk_fma_f32 v[48:49], v[182:183], v[48:49], v[150:151]
	v_pk_fma_f32 v[50:51], v[184:185], v[50:51], v[152:153]
	v_cvt_pk_bf16_f32 v88, v48, v49
	v_cvt_pk_bf16_f32 v89, v50, v51
	global_store_dwordx2 v35, v[88:89], s[8:9] offset:1024
	s_waitcnt vmcnt(19)
	v_pk_mul_f32 v[52:53], v[52:53], v[80:81] op_sel_hi:[1,0]
	v_pk_mul_f32 v[54:55], v[54:55], v[80:81] op_sel_hi:[1,0]
	v_pk_add_f32 v[186:187], v[186:187], 1.0 op_sel_hi:[1,0]
	v_pk_add_f32 v[188:189], v[188:189], 1.0 op_sel_hi:[1,0]
	v_pk_mul_f32 v[52:53], v[122:123], v[52:53]
	v_pk_mul_f32 v[54:55], v[124:125], v[54:55]
	v_pk_fma_f32 v[52:53], v[186:187], v[52:53], v[154:155]
	v_pk_fma_f32 v[54:55], v[188:189], v[54:55], v[156:157]
	v_cvt_pk_bf16_f32 v90, v52, v53
	v_cvt_pk_bf16_f32 v91, v54, v55
	global_store_dwordx2 v35, v[90:91], s[8:9] offset:1536
	s_waitcnt vmcnt(18)
	v_pk_mul_f32 v[56:57], v[56:57], v[80:81] op_sel_hi:[1,0]
	v_pk_mul_f32 v[58:59], v[58:59], v[80:81] op_sel_hi:[1,0]
	v_pk_add_f32 v[190:191], v[190:191], 1.0 op_sel_hi:[1,0]
	v_pk_add_f32 v[192:193], v[192:193], 1.0 op_sel_hi:[1,0]
	v_pk_mul_f32 v[56:57], v[126:127], v[56:57]
	v_pk_mul_f32 v[58:59], v[128:129], v[58:59]
	v_pk_fma_f32 v[56:57], v[190:191], v[56:57], v[158:159]
	v_pk_fma_f32 v[58:59], v[192:193], v[58:59], v[160:161]
	v_cvt_pk_bf16_f32 v92, v56, v57
	v_cvt_pk_bf16_f32 v93, v58, v59
	global_store_dwordx2 v35, v[92:93], s[8:9] offset:2048
	s_waitcnt vmcnt(17)
	v_pk_mul_f32 v[60:61], v[60:61], v[80:81] op_sel_hi:[1,0]
	v_pk_mul_f32 v[62:63], v[62:63], v[80:81] op_sel_hi:[1,0]
	v_pk_add_f32 v[194:195], v[194:195], 1.0 op_sel_hi:[1,0]
	v_pk_add_f32 v[196:197], v[196:197], 1.0 op_sel_hi:[1,0]
	v_pk_mul_f32 v[60:61], v[130:131], v[60:61]
	v_pk_mul_f32 v[62:63], v[132:133], v[62:63]
	v_pk_fma_f32 v[60:61], v[194:195], v[60:61], v[162:163]
	v_pk_fma_f32 v[62:63], v[196:197], v[62:63], v[164:165]
	v_cvt_pk_bf16_f32 v94, v60, v61
	v_cvt_pk_bf16_f32 v95, v62, v63
	global_store_dwordx2 v35, v[94:95], s[8:9] offset:2560
	s_waitcnt vmcnt(16)
	v_pk_mul_f32 v[64:65], v[64:65], v[80:81] op_sel_hi:[1,0]
	v_pk_mul_f32 v[66:67], v[66:67], v[80:81] op_sel_hi:[1,0]
	v_pk_add_f32 v[198:199], v[198:199], 1.0 op_sel_hi:[1,0]
	v_pk_add_f32 v[200:201], v[200:201], 1.0 op_sel_hi:[1,0]
	v_pk_mul_f32 v[64:65], v[134:135], v[64:65]
	v_pk_mul_f32 v[66:67], v[136:137], v[66:67]
	v_pk_fma_f32 v[64:65], v[198:199], v[64:65], v[166:167]
	v_pk_fma_f32 v[66:67], v[200:201], v[66:67], v[168:169]
	v_cvt_pk_bf16_f32 v96, v64, v65
	v_cvt_pk_bf16_f32 v97, v66, v67
	global_store_dwordx2 v35, v[96:97], s[8:9] offset:3072
	s_waitcnt vmcnt(15)
	v_pk_mul_f32 v[68:69], v[68:69], v[80:81] op_sel_hi:[1,0]
	v_pk_mul_f32 v[70:71], v[70:71], v[80:81] op_sel_hi:[1,0]
	v_pk_add_f32 v[202:203], v[202:203], 1.0 op_sel_hi:[1,0]
	v_pk_add_f32 v[204:205], v[204:205], 1.0 op_sel_hi:[1,0]
	v_pk_mul_f32 v[68:69], v[138:139], v[68:69]
	v_pk_mul_f32 v[70:71], v[140:141], v[70:71]
	v_pk_fma_f32 v[68:69], v[202:203], v[68:69], v[170:171]
	v_pk_fma_f32 v[70:71], v[204:205], v[70:71], v[172:173]
	v_cvt_pk_bf16_f32 v98, v68, v69
	v_cvt_pk_bf16_f32 v99, v70, v71
	global_store_dwordx2 v35, v[98:99], s[8:9] offset:3584
	s_add_i32 s13, s13, 0x800
	s_cmp_ge_u32 s13, 0x2400
	s_cbranch_scc1 .Ln0_done
; DI unsigned pk_bf16(float lo, float hi) { f32x2 v = {lo, hi}; hbf16x2 r = __builtin_convertvector(v, hbf16x2); return __builtin_bit_cast(unsigned, r); }
; DI void norm_mod_store(const f32x4 (&v)[8], const float* gain, const float* shift, const float* scale, bf16_t* hrow, int lane, unsigned char* h8row = nullptr) {
;     float ss = 0.f;
; #pragma unroll
;     for (int i = 0; i < 8; ++i) ss += v[i][0] * v[i][0] + v[i][1] * v[i][1] + v[i][2] * v[i][2] + v[i][3] * v[i][3];
;     ss = wave_sum(ss);
;     const float r = rsqrtf(ss * (1.0f / DM) + EPS);
; #pragma unroll
;     for (int i = 0; i < 8; ++i) {
;         const int col = 4 * lane + 256 * i;
;         const f32x4 g = *(const f32x4*)(gain + col), sh = *(const f32x4*)(shift + col), sc = *(const f32x4*)(scale + col);
;         const f32x4 h = (v[i] * r * g) * (1.0f + sc) + sh;
;         if (h8row) *(unsigned*)(h8row + col) = pk_fp8x4(h[0], h[1], h[2], h[3]);
;         else { u32x2 w; w.x = pk_bf16(h[0], h[1]); w.y = pk_bf16(h[2], h[3]); *(u32x2*)(hrow + col) = w; }
;     }
; DI void phase_norm0(const Params& p, int G, int bid) {
;     ...
;     for (int row = bid * 8 + wave; row < NTOK; row += G * 8) {
;         const float* xr = row < NCTX ? p.in[2] + (size_t)row * DM : p.in[0] + (size_t)(row - NCTX) * DM;
;         f32x4 v[8];
; #pragma unroll
;         for (int i = 0; i < 8; ++i) v[i] = *(const f32x4*)(xr + 4 * lane + 256 * i);
;         const float* md = MOD + (size_t)row_mod(row) * MODN;
;         norm_mod_store(v, p.in[9], md, md + DM, H + (size_t)row * DM, lane);
;     }
	s_sub_i32 s15, s13, 0x400
	s_lshr_b32 s15, s15, 11
	s_cmp_lt_u32 s13, 0x400
	s_cselect_b32 s15, 4, s15
	s_mul_i32 s15, s15, 0xc000
	s_add_u32 s4, s50, s15
	s_addc_u32 s5, s51, 0
	s_add_u32 s4, s4, 0x10000
	s_addc_u32 s5, s5, 0
	s_add_u32 s6, s4, 0x2000
	s_addc_u32 s7, s5, 0
	s_lshl_b32 s15, s13, 12
	s_add_u32 s8, s50, s15
	s_addc_u32 s9, s51, 0
	s_add_u32 s8, s8, 0x2420e000
	s_addc_u32 s9, s9, 0
	global_load_dwordx4 v[142:145], v1, s[4:5] offset:0
	global_load_dwordx4 v[174:177], v1, s[6:7] offset:0
	global_load_dwordx4 v[146:149], v1, s[4:5] offset:1024
	global_load_dwordx4 v[178:181], v1, s[6:7] offset:1024
	global_load_dwordx4 v[150:153], v1, s[4:5] offset:2048
	global_load_dwordx4 v[182:185], v1, s[6:7] offset:2048
	global_load_dwordx4 v[154:157], v1, s[4:5] offset:3072
	global_load_dwordx4 v[186:189], v1, s[6:7] offset:3072
	global_load_dwordx4 v[158:161], v34, s[4:5] offset:0
	global_load_dwordx4 v[190:193], v34, s[6:7] offset:0
	global_load_dwordx4 v[162:165], v34, s[4:5] offset:1024
	global_load_dwordx4 v[194:197], v34, s[6:7] offset:1024
	global_load_dwordx4 v[166:169], v34, s[4:5] offset:2048
	global_load_dwordx4 v[198:201], v34, s[6:7] offset:2048
	global_load_dwordx4 v[170:173], v34, s[4:5] offset:3072
	global_load_dwordx4 v[202:205], v34, s[6:7] offset:3072
	s_add_i32 s16, s13, 0x800
	s_cmp_ge_u32 s16, 0x2400
	s_cselect_b32 s16, s13, s16
	s_sub_i32 s15, s16, 0x400
	s_cmp_lt_u32 s16, 0x400
	s_cselect_b32 s15, s16, s15
	s_cselect_b32 s2, s56, s52
	s_cselect_b32 s3, s57, s53
	s_lshl_b32 s15, s15, 13
	s_add_u32 s2, s2, s15
	s_addc_u32 s3, s3, 0
	global_load_dwordx4 v[40:43], v1, s[2:3] offset:0 nt
	global_load_dwordx4 v[44:47], v1, s[2:3] offset:1024 nt
	global_load_dwordx4 v[48:51], v1, s[2:3] offset:2048 nt
	global_load_dwordx4 v[52:55], v1, s[2:3] offset:3072 nt
	global_load_dwordx4 v[56:59], v34, s[2:3] offset:0 nt
	global_load_dwordx4 v[60:63], v34, s[2:3] offset:1024 nt
	global_load_dwordx4 v[64:67], v34, s[2:3] offset:2048 nt
	global_load_dwordx4 v[68:71], v34, s[2:3] offset:3072 nt
	s_waitcnt vmcnt(32)
	v_mul_f32_e32 v80, v3, v3
	v_fmac_f32_e32 v80, v2, v2
	v_fmac_f32_e32 v80, v4, v4
	v_fmac_f32_e32 v80, v5, v5
	v_mul_f32_e32 v82, v7, v7
	v_fmac_f32_e32 v82, v6, v6
	v_fmac_f32_e32 v82, v8, v8
	v_fmac_f32_e32 v82, v9, v9
	v_add_f32_e32 v80, v80, v82
	v_mul_f32_e32 v82, v11, v11
	v_fmac_f32_e32 v82, v10, v10
	v_fmac_f32_e32 v82, v12, v12
	v_fmac_f32_e32 v82, v13, v13
	v_add_f32_e32 v80, v80, v82
	v_mul_f32_e32 v82, v15, v15
	v_fmac_f32_e32 v82, v14, v14
	v_fmac_f32_e32 v82, v16, v16
	v_fmac_f32_e32 v82, v17, v17
	v_add_f32_e32 v80, v80, v82
	v_mul_f32_e32 v82, v19, v19
	v_fmac_f32_e32 v82, v18, v18
	v_fmac_f32_e32 v82, v20, v20
	v_fmac_f32_e32 v82, v21, v21
	v_add_f32_e32 v80, v80, v82
	v_mul_f32_e32 v82, v23, v23
	v_fmac_f32_e32 v82, v22, v22
	v_fmac_f32_e32 v82, v24, v24
	v_fmac_f32_e32 v82, v25, v25
	v_add_f32_e32 v80, v80, v82
	v_mul_f32_e32 v82, v27, v27
	v_fmac_f32_e32 v82, v26, v26
	v_fmac_f32_e32 v82, v28, v28
	v_fmac_f32_e32 v82, v29, v29
	v_add_f32_e32 v80, v80, v82
	v_mul_f32_e32 v82, v31, v31
	v_fmac_f32_e32 v82, v30, v30
	v_fmac_f32_e32 v82, v32, v32
	v_fmac_f32_e32 v82, v33, v33
	v_add_f32_e32 v80, v80, v82
	ds_bpermute_b32 v82, v72, v80
	s_waitcnt lgkmcnt(0)
	v_add_f32_e32 v80, v80, v82
	ds_bpermute_b32 v82, v73, v80
	s_waitcnt lgkmcnt(0)
	v_add_f32_e32 v80, v80, v82
	ds_bpermute_b32 v82, v74, v80
	s_waitcnt lgkmcnt(0)
	v_add_f32_e32 v80, v80, v82
	ds_bpermute_b32 v82, v75, v80
	s_waitcnt lgkmcnt(0)
	v_add_f32_e32 v80, v80, v82
	ds_bpermute_b32 v82, v76, v80
	s_waitcnt lgkmcnt(0)
	v_add_f32_e32 v80, v80, v82
	ds_bpermute_b32 v82, v77, v80
	s_waitcnt lgkmcnt(0)
	v_add_f32_e32 v80, v80, v82
	v_mov_b32_e32 v83, 0x358637bd
	v_fmamk_f32 v80, v80, 0x3a000000, v83
	v_cmp_gt_f32_e32 vcc, 0x800000, v80
	v_mul_f32_e32 v82, 0x4b800000, v80
	s_nop 1
	v_cndmask_b32_e32 v80, v80, v82, vcc
	v_rsq_f32_e32 v80, v80
	s_nop 0
	v_mul_f32_e32 v82, 0x45800000, v80
	s_nop 0
	v_cndmask_b32_e32 v80, v80, v82, vcc
	s_waitcnt vmcnt(22)
	v_pk_mul_f32 v[2:3], v[2:3], v[80:81] op_sel_hi:[1,0]
	v_pk_mul_f32 v[4:5], v[4:5], v[80:81] op_sel_hi:[1,0]
	v_pk_add_f32 v[174:175], v[174:175], 1.0 op_sel_hi:[1,0]
	v_pk_add_f32 v[176:177], v[176:177], 1.0 op_sel_hi:[1,0]
	v_pk_mul_f32 v[2:3], v[110:111], v[2:3]
	v_pk_mul_f32 v[4:5], v[112:113], v[4:5]
	v_pk_fma_f32 v[2:3], v[174:175], v[2:3], v[142:143]
	v_pk_fma_f32 v[4:5], v[176:177], v[4:5], v[144:145]
	v_cvt_pk_bf16_f32 v84, v2, v3
	v_cvt_pk_bf16_f32 v85, v4, v5
	global_store_dwordx2 v35, v[84:85], s[8:9] offset:0
	s_waitcnt vmcnt(21)
	v_pk_mul_f32 v[6:7], v[6:7], v[80:81] op_sel_hi:[1,0]
	v_pk_mul_f32 v[8:9], v[8:9], v[80:81] op_sel_hi:[1,0]
	v_pk_add_f32 v[178:179], v[178:179], 1.0 op_sel_hi:[1,0]
	v_pk_add_f32 v[180:181], v[180:181], 1.0 op_sel_hi:[1,0]
	v_pk_mul_f32 v[6:7], v[114:115], v[6:7]
	v_pk_mul_f32 v[8:9], v[116:117], v[8:9]
	v_pk_fma_f32 v[6:7], v[178:179], v[6:7], v[146:147]
	v_pk_fma_f32 v[8:9], v[180:181], v[8:9], v[148:149]
	v_cvt_pk_bf16_f32 v86, v6, v7
	v_cvt_pk_bf16_f32 v87, v8, v9
	global_store_dwordx2 v35, v[86:87], s[8:9] offset:512
	s_waitcnt vmcnt(20)
	v_pk_mul_f32 v[10:11], v[10:11], v[80:81] op_sel_hi:[1,0]
	v_pk_mul_f32 v[12:13], v[12:13], v[80:81] op_sel_hi:[1,0]
	v_pk_add_f32 v[182:183], v[182:183], 1.0 op_sel_hi:[1,0]
	v_pk_add_f32 v[184:185], v[184:185], 1.0 op_sel_hi:[1,0]
	v_pk_mul_f32 v[10:11], v[118:119], v[10:11]
	v_pk_mul_f32 v[12:13], v[120:121], v[12:13]
	v_pk_fma_f32 v[10:11], v[182:183], v[10:11], v[150:151]
	v_pk_fma_f32 v[12:13], v[184:185], v[12:13], v[152:153]
	v_cvt_pk_bf16_f32 v88, v10, v11
	v_cvt_pk_bf16_f32 v89, v12, v13
	global_store_dwordx2 v35, v[88:89], s[8:9] offset:1024
	s_waitcnt vmcnt(19)
; DI unsigned pk_bf16(float lo, float hi) { f32x2 v = {lo, hi}; hbf16x2 r = __builtin_convertvector(v, hbf16x2); return __builtin_bit_cast(unsigned, r); }
; DI void norm_mod_store(const f32x4 (&v)[8], const float* gain, const float* shift, const float* scale, bf16_t* hrow, int lane, unsigned char* h8row = nullptr) {
;     ...
;     const float r = rsqrtf(ss * (1.0f / DM) + EPS);
; #pragma unroll
;     for (int i = 0; i < 8; ++i) {
;         const int col = 4 * lane + 256 * i;
;         const f32x4 g = *(const f32x4*)(gain + col), sh = *(const f32x4*)(shift + col), sc = *(const f32x4*)(scale + col);
;         const f32x4 h = (v[i] * r * g) * (1.0f + sc) + sh;
;         if (h8row) *(unsigned*)(h8row + col) = pk_fp8x4(h[0], h[1], h[2], h[3]);
;         else { u32x2 w; w.x = pk_bf16(h[0], h[1]); w.y = pk_bf16(h[2], h[3]); *(u32x2*)(hrow + col) = w; }
;     }
; DI void phase_norm0(const Params& p, int G, int bid) {
;     ...
;     for (int row = bid * 8 + wave; row < NTOK; row += G * 8) {
;         const float* xr = row < NCTX ? p.in[2] + (size_t)row * DM : p.in[0] + (size_t)(row - NCTX) * DM;
;         f32x4 v[8];
; #pragma unroll
;         for (int i = 0; i < 8; ++i) v[i] = *(const f32x4*)(xr + 4 * lane + 256 * i);
;         const float* md = MOD + (size_t)row_mod(row) * MODN;
;         norm_mod_store(v, p.in[9], md, md + DM, H + (size_t)row * DM, lane);
;     }
	v_pk_mul_f32 v[14:15], v[14:15], v[80:81] op_sel_hi:[1,0]
	v_pk_mul_f32 v[16:17], v[16:17], v[80:81] op_sel_hi:[1,0]
	v_pk_add_f32 v[186:187], v[186:187], 1.0 op_sel_hi:[1,0]
	v_pk_add_f32 v[188:189], v[188:189], 1.0 op_sel_hi:[1,0]
	v_pk_mul_f32 v[14:15], v[122:123], v[14:15]
	v_pk_mul_f32 v[16:17], v[124:125], v[16:17]
	v_pk_fma_f32 v[14:15], v[186:187], v[14:15], v[154:155]
	v_pk_fma_f32 v[16:17], v[188:189], v[16:17], v[156:157]
	v_cvt_pk_bf16_f32 v90, v14, v15
	v_cvt_pk_bf16_f32 v91, v16, v17
	global_store_dwordx2 v35, v[90:91], s[8:9] offset:1536
	s_waitcnt vmcnt(18)
	v_pk_mul_f32 v[18:19], v[18:19], v[80:81] op_sel_hi:[1,0]
	v_pk_mul_f32 v[20:21], v[20:21], v[80:81] op_sel_hi:[1,0]
	v_pk_add_f32 v[190:191], v[190:191], 1.0 op_sel_hi:[1,0]
	v_pk_add_f32 v[192:193], v[192:193], 1.0 op_sel_hi:[1,0]
	v_pk_mul_f32 v[18:19], v[126:127], v[18:19]
	v_pk_mul_f32 v[20:21], v[128:129], v[20:21]
	v_pk_fma_f32 v[18:19], v[190:191], v[18:19], v[158:159]
	v_pk_fma_f32 v[20:21], v[192:193], v[20:21], v[160:161]
	v_cvt_pk_bf16_f32 v92, v18, v19
	v_cvt_pk_bf16_f32 v93, v20, v21
	global_store_dwordx2 v35, v[92:93], s[8:9] offset:2048
	s_waitcnt vmcnt(17)
	v_pk_mul_f32 v[22:23], v[22:23], v[80:81] op_sel_hi:[1,0]
	v_pk_mul_f32 v[24:25], v[24:25], v[80:81] op_sel_hi:[1,0]
	v_pk_add_f32 v[194:195], v[194:195], 1.0 op_sel_hi:[1,0]
	v_pk_add_f32 v[196:197], v[196:197], 1.0 op_sel_hi:[1,0]
	v_pk_mul_f32 v[22:23], v[130:131], v[22:23]
	v_pk_mul_f32 v[24:25], v[132:133], v[24:25]
	v_pk_fma_f32 v[22:23], v[194:195], v[22:23], v[162:163]
	v_pk_fma_f32 v[24:25], v[196:197], v[24:25], v[164:165]
	v_cvt_pk_bf16_f32 v94, v22, v23
	v_cvt_pk_bf16_f32 v95, v24, v25
	global_store_dwordx2 v35, v[94:95], s[8:9] offset:2560
	s_waitcnt vmcnt(16)
	v_pk_mul_f32 v[26:27], v[26:27], v[80:81] op_sel_hi:[1,0]
	v_pk_mul_f32 v[28:29], v[28:29], v[80:81] op_sel_hi:[1,0]
	v_pk_add_f32 v[198:199], v[198:199], 1.0 op_sel_hi:[1,0]
	v_pk_add_f32 v[200:201], v[200:201], 1.0 op_sel_hi:[1,0]
	v_pk_mul_f32 v[26:27], v[134:135], v[26:27]
	v_pk_mul_f32 v[28:29], v[136:137], v[28:29]
	v_pk_fma_f32 v[26:27], v[198:199], v[26:27], v[166:167]
	v_pk_fma_f32 v[28:29], v[200:201], v[28:29], v[168:169]
	v_cvt_pk_bf16_f32 v96, v26, v27
	v_cvt_pk_bf16_f32 v97, v28, v29
	global_store_dwordx2 v35, v[96:97], s[8:9] offset:3072
	s_waitcnt vmcnt(15)
	v_pk_mul_f32 v[30:31], v[30:31], v[80:81] op_sel_hi:[1,0]
	v_pk_mul_f32 v[32:33], v[32:33], v[80:81] op_sel_hi:[1,0]
	v_pk_add_f32 v[202:203], v[202:203], 1.0 op_sel_hi:[1,0]
	v_pk_add_f32 v[204:205], v[204:205], 1.0 op_sel_hi:[1,0]
	v_pk_mul_f32 v[30:31], v[138:139], v[30:31]
	v_pk_mul_f32 v[32:33], v[140:141], v[32:33]
	v_pk_fma_f32 v[30:31], v[202:203], v[30:31], v[170:171]
	v_pk_fma_f32 v[32:33], v[204:205], v[32:33], v[172:173]
	v_cvt_pk_bf16_f32 v98, v30, v31
	v_cvt_pk_bf16_f32 v99, v32, v33
	global_store_dwordx2 v35, v[98:99], s[8:9] offset:3584
	s_add_i32 s13, s13, 0x800
	s_cmp_ge_u32 s13, 0x2400
	s_cbranch_scc1 .Ln0_done
	s_sub_i32 s15, s13, 0x400
	s_lshr_b32 s15, s15, 11
	s_cmp_lt_u32 s13, 0x400
	s_cselect_b32 s15, 4, s15
	s_mul_i32 s15, s15, 0xc000
	s_add_u32 s4, s50, s15
	s_addc_u32 s5, s51, 0
	s_add_u32 s4, s4, 0x10000
	s_addc_u32 s5, s5, 0
	s_add_u32 s6, s4, 0x2000
	s_addc_u32 s7, s5, 0
	s_lshl_b32 s15, s13, 12
	s_add_u32 s8, s50, s15
	s_addc_u32 s9, s51, 0
	s_add_u32 s8, s8, 0x2420e000
	s_addc_u32 s9, s9, 0
	global_load_dwordx4 v[142:145], v1, s[4:5] offset:0
	global_load_dwordx4 v[174:177], v1, s[6:7] offset:0
	global_load_dwordx4 v[146:149], v1, s[4:5] offset:1024
	global_load_dwordx4 v[178:181], v1, s[6:7] offset:1024
	global_load_dwordx4 v[150:153], v1, s[4:5] offset:2048
	global_load_dwordx4 v[182:185], v1, s[6:7] offset:2048
	global_load_dwordx4 v[154:157], v1, s[4:5] offset:3072
	global_load_dwordx4 v[186:189], v1, s[6:7] offset:3072
	global_load_dwordx4 v[158:161], v34, s[4:5] offset:0
	global_load_dwordx4 v[190:193], v34, s[6:7] offset:0
	global_load_dwordx4 v[162:165], v34, s[4:5] offset:1024
	global_load_dwordx4 v[194:197], v34, s[6:7] offset:1024
	global_load_dwordx4 v[166:169], v34, s[4:5] offset:2048
	global_load_dwordx4 v[198:201], v34, s[6:7] offset:2048
	global_load_dwordx4 v[170:173], v34, s[4:5] offset:3072
	global_load_dwordx4 v[202:205], v34, s[6:7] offset:3072
	s_add_i32 s16, s13, 0x800
	s_cmp_ge_u32 s16, 0x2400
	s_cselect_b32 s16, s13, s16
	s_sub_i32 s15, s16, 0x400
	s_cmp_lt_u32 s16, 0x400
	s_cselect_b32 s15, s16, s15
	s_cselect_b32 s2, s56, s52
	s_cselect_b32 s3, s57, s53
	s_lshl_b32 s15, s15, 13
	s_add_u32 s2, s2, s15
	s_addc_u32 s3, s3, 0
	global_load_dwordx4 v[2:5], v1, s[2:3] offset:0 nt
	global_load_dwordx4 v[6:9], v1, s[2:3] offset:1024 nt
	global_load_dwordx4 v[10:13], v1, s[2:3] offset:2048 nt
	global_load_dwordx4 v[14:17], v1, s[2:3] offset:3072 nt
	global_load_dwordx4 v[18:21], v34, s[2:3] offset:0 nt
	global_load_dwordx4 v[22:25], v34, s[2:3] offset:1024 nt
	global_load_dwordx4 v[26:29], v34, s[2:3] offset:2048 nt
	global_load_dwordx4 v[30:33], v34, s[2:3] offset:3072 nt
	s_waitcnt vmcnt(32)
	v_mul_f32_e32 v80, v41, v41
	v_fmac_f32_e32 v80, v40, v40
	v_fmac_f32_e32 v80, v42, v42
	v_fmac_f32_e32 v80, v43, v43
	v_mul_f32_e32 v82, v45, v45
	v_fmac_f32_e32 v82, v44, v44
	v_fmac_f32_e32 v82, v46, v46
	v_fmac_f32_e32 v82, v47, v47
	v_add_f32_e32 v80, v80, v82
	v_mul_f32_e32 v82, v49, v49
	v_fmac_f32_e32 v82, v48, v48
	v_fmac_f32_e32 v82, v50, v50
	v_fmac_f32_e32 v82, v51, v51
	v_add_f32_e32 v80, v80, v82
	v_mul_f32_e32 v82, v53, v53
	v_fmac_f32_e32 v82, v52, v52
	v_fmac_f32_e32 v82, v54, v54
	v_fmac_f32_e32 v82, v55, v55
	v_add_f32_e32 v80, v80, v82
	v_mul_f32_e32 v82, v57, v57
	v_fmac_f32_e32 v82, v56, v56
	v_fmac_f32_e32 v82, v58, v58
	v_fmac_f32_e32 v82, v59, v59
	v_add_f32_e32 v80, v80, v82
	v_mul_f32_e32 v82, v61, v61
	v_fmac_f32_e32 v82, v60, v60
	v_fmac_f32_e32 v82, v62, v62
	v_fmac_f32_e32 v82, v63, v63
	v_add_f32_e32 v80, v80, v82
	v_mul_f32_e32 v82, v65, v65
	v_fmac_f32_e32 v82, v64, v64
	v_fmac_f32_e32 v82, v66, v66
	v_fmac_f32_e32 v82, v67, v67
	v_add_f32_e32 v80, v80, v82
	v_mul_f32_e32 v82, v69, v69
	v_fmac_f32_e32 v82, v68, v68
	v_fmac_f32_e32 v82, v70, v70
	v_fmac_f32_e32 v82, v71, v71
	v_add_f32_e32 v80, v80, v82
	ds_bpermute_b32 v82, v72, v80
	s_waitcnt lgkmcnt(0)
; DI unsigned pk_bf16(float lo, float hi) { f32x2 v = {lo, hi}; hbf16x2 r = __builtin_convertvector(v, hbf16x2); return __builtin_bit_cast(unsigned, r); }
; DI void norm_mod_store(const f32x4 (&v)[8], const float* gain, const float* shift, const float* scale, bf16_t* hrow, int lane, unsigned char* h8row = nullptr) {
;     ...
;     const float r = rsqrtf(ss * (1.0f / DM) + EPS);
; #pragma unroll
;     for (int i = 0; i < 8; ++i) {
;         const int col = 4 * lane + 256 * i;
;         const f32x4 g = *(const f32x4*)(gain + col), sh = *(const f32x4*)(shift + col), sc = *(const f32x4*)(scale + col);
;         const f32x4 h = (v[i] * r * g) * (1.0f + sc) + sh;
;         if (h8row) *(unsigned*)(h8row + col) = pk_fp8x4(h[0], h[1], h[2], h[3]);
;         else { u32x2 w; w.x = pk_bf16(h[0], h[1]); w.y = pk_bf16(h[2], h[3]); *(u32x2*)(hrow + col) = w; }
;     }
	v_add_f32_e32 v80, v80, v82
	ds_bpermute_b32 v82, v73, v80
	s_waitcnt lgkmcnt(0)
	v_add_f32_e32 v80, v80, v82
	ds_bpermute_b32 v82, v74, v80
	s_waitcnt lgkmcnt(0)
	v_add_f32_e32 v80, v80, v82
	ds_bpermute_b32 v82, v75, v80
	s_waitcnt lgkmcnt(0)
	v_add_f32_e32 v80, v80, v82
	ds_bpermute_b32 v82, v76, v80
	s_waitcnt lgkmcnt(0)
	v_add_f32_e32 v80, v80, v82
	ds_bpermute_b32 v82, v77, v80
	s_waitcnt lgkmcnt(0)
	v_add_f32_e32 v80, v80, v82
	v_mov_b32_e32 v83, 0x358637bd
	v_fmamk_f32 v80, v80, 0x3a000000, v83
	v_cmp_gt_f32_e32 vcc, 0x800000, v80
	v_mul_f32_e32 v82, 0x4b800000, v80
	s_nop 1
	v_cndmask_b32_e32 v80, v80, v82, vcc
	v_rsq_f32_e32 v80, v80
	s_nop 0
	v_mul_f32_e32 v82, 0x45800000, v80
	s_nop 0
	v_cndmask_b32_e32 v80, v80, v82, vcc
	s_waitcnt vmcnt(22)
	v_pk_mul_f32 v[40:41], v[40:41], v[80:81] op_sel_hi:[1,0]
	v_pk_mul_f32 v[42:43], v[42:43], v[80:81] op_sel_hi:[1,0]
	v_pk_add_f32 v[174:175], v[174:175], 1.0 op_sel_hi:[1,0]
	v_pk_add_f32 v[176:177], v[176:177], 1.0 op_sel_hi:[1,0]
	v_pk_mul_f32 v[40:41], v[110:111], v[40:41]
	v_pk_mul_f32 v[42:43], v[112:113], v[42:43]
	v_pk_fma_f32 v[40:41], v[174:175], v[40:41], v[142:143]
	v_pk_fma_f32 v[42:43], v[176:177], v[42:43], v[144:145]
	v_cvt_pk_bf16_f32 v84, v40, v41
	v_cvt_pk_bf16_f32 v85, v42, v43
	global_store_dwordx2 v35, v[84:85], s[8:9] offset:0
	s_waitcnt vmcnt(21)
	v_pk_mul_f32 v[44:45], v[44:45], v[80:81] op_sel_hi:[1,0]
	v_pk_mul_f32 v[46:47], v[46:47], v[80:81] op_sel_hi:[1,0]
	v_pk_add_f32 v[178:179], v[178:179], 1.0 op_sel_hi:[1,0]
	v_pk_add_f32 v[180:181], v[180:181], 1.0 op_sel_hi:[1,0]
	v_pk_mul_f32 v[44:45], v[114:115], v[44:45]
	v_pk_mul_f32 v[46:47], v[116:117], v[46:47]
	v_pk_fma_f32 v[44:45], v[178:179], v[44:45], v[146:147]
	v_pk_fma_f32 v[46:47], v[180:181], v[46:47], v[148:149]
	v_cvt_pk_bf16_f32 v86, v44, v45
	v_cvt_pk_bf16_f32 v87, v46, v47
	global_store_dwordx2 v35, v[86:87], s[8:9] offset:512
	s_waitcnt vmcnt(20)
	v_pk_mul_f32 v[48:49], v[48:49], v[80:81] op_sel_hi:[1,0]
	v_pk_mul_f32 v[50:51], v[50:51], v[80:81] op_sel_hi:[1,0]
	v_pk_add_f32 v[182:183], v[182:183], 1.0 op_sel_hi:[1,0]
	v_pk_add_f32 v[184:185], v[184:185], 1.0 op_sel_hi:[1,0]
	v_pk_mul_f32 v[48:49], v[118:119], v[48:49]
	v_pk_mul_f32 v[50:51], v[120:121], v[50:51]
	v_pk_fma_f32 v[48:49], v[182:183], v[48:49], v[150:151]
	v_pk_fma_f32 v[50:51], v[184:185], v[50:51], v[152:153]
	v_cvt_pk_bf16_f32 v88, v48, v49
	v_cvt_pk_bf16_f32 v89, v50, v51
	global_store_dwordx2 v35, v[88:89], s[8:9] offset:1024
	s_waitcnt vmcnt(19)
	v_pk_mul_f32 v[52:53], v[52:53], v[80:81] op_sel_hi:[1,0]
	v_pk_mul_f32 v[54:55], v[54:55], v[80:81] op_sel_hi:[1,0]
	v_pk_add_f32 v[186:187], v[186:187], 1.0 op_sel_hi:[1,0]
	v_pk_add_f32 v[188:189], v[188:189], 1.0 op_sel_hi:[1,0]
	v_pk_mul_f32 v[52:53], v[122:123], v[52:53]
	v_pk_mul_f32 v[54:55], v[124:125], v[54:55]
	v_pk_fma_f32 v[52:53], v[186:187], v[52:53], v[154:155]
	v_pk_fma_f32 v[54:55], v[188:189], v[54:55], v[156:157]
	v_cvt_pk_bf16_f32 v90, v52, v53
	v_cvt_pk_bf16_f32 v91, v54, v55
	global_store_dwordx2 v35, v[90:91], s[8:9] offset:1536
	s_waitcnt vmcnt(18)
	v_pk_mul_f32 v[56:57], v[56:57], v[80:81] op_sel_hi:[1,0]
	v_pk_mul_f32 v[58:59], v[58:59], v[80:81] op_sel_hi:[1,0]
	v_pk_add_f32 v[190:191], v[190:191], 1.0 op_sel_hi:[1,0]
	v_pk_add_f32 v[192:193], v[192:193], 1.0 op_sel_hi:[1,0]
	v_pk_mul_f32 v[56:57], v[126:127], v[56:57]
	v_pk_mul_f32 v[58:59], v[128:129], v[58:59]
	v_pk_fma_f32 v[56:57], v[190:191], v[56:57], v[158:159]
	v_pk_fma_f32 v[58:59], v[192:193], v[58:59], v[160:161]
	v_cvt_pk_bf16_f32 v92, v56, v57
	v_cvt_pk_bf16_f32 v93, v58, v59
	global_store_dwordx2 v35, v[92:93], s[8:9] offset:2048
	s_waitcnt vmcnt(17)
	v_pk_mul_f32 v[60:61], v[60:61], v[80:81] op_sel_hi:[1,0]
	v_pk_mul_f32 v[62:63], v[62:63], v[80:81] op_sel_hi:[1,0]
	v_pk_add_f32 v[194:195], v[194:195], 1.0 op_sel_hi:[1,0]
	v_pk_add_f32 v[196:197], v[196:197], 1.0 op_sel_hi:[1,0]
	v_pk_mul_f32 v[60:61], v[130:131], v[60:61]
	v_pk_mul_f32 v[62:63], v[132:133], v[62:63]
	v_pk_fma_f32 v[60:61], v[194:195], v[60:61], v[162:163]
	v_pk_fma_f32 v[62:63], v[196:197], v[62:63], v[164:165]
	v_cvt_pk_bf16_f32 v94, v60, v61
	v_cvt_pk_bf16_f32 v95, v62, v63
	global_store_dwordx2 v35, v[94:95], s[8:9] offset:2560
	s_waitcnt vmcnt(16)
	v_pk_mul_f32 v[64:65], v[64:65], v[80:81] op_sel_hi:[1,0]
	v_pk_mul_f32 v[66:67], v[66:67], v[80:81] op_sel_hi:[1,0]
	v_pk_add_f32 v[198:199], v[198:199], 1.0 op_sel_hi:[1,0]
	v_pk_add_f32 v[200:201], v[200:201], 1.0 op_sel_hi:[1,0]
	v_pk_mul_f32 v[64:65], v[134:135], v[64:65]
	v_pk_mul_f32 v[66:67], v[136:137], v[66:67]
	v_pk_fma_f32 v[64:65], v[198:199], v[64:65], v[166:167]
	v_pk_fma_f32 v[66:67], v[200:201], v[66:67], v[168:169]
	v_cvt_pk_bf16_f32 v96, v64, v65
	v_cvt_pk_bf16_f32 v97, v66, v67
	global_store_dwordx2 v35, v[96:97], s[8:9] offset:3072
	s_waitcnt vmcnt(15)
	v_pk_mul_f32 v[68:69], v[68:69], v[80:81] op_sel_hi:[1,0]
	v_pk_mul_f32 v[70:71], v[70:71], v[80:81] op_sel_hi:[1,0]
	v_pk_add_f32 v[202:203], v[202:203], 1.0 op_sel_hi:[1,0]
	v_pk_add_f32 v[204:205], v[204:205], 1.0 op_sel_hi:[1,0]
	v_pk_mul_f32 v[68:69], v[138:139], v[68:69]
	v_pk_mul_f32 v[70:71], v[140:141], v[70:71]
	v_pk_fma_f32 v[68:69], v[202:203], v[68:69], v[170:171]
	v_pk_fma_f32 v[70:71], v[204:205], v[70:71], v[172:173]
	v_cvt_pk_bf16_f32 v98, v68, v69
	v_cvt_pk_bf16_f32 v99, v70, v71
	global_store_dwordx2 v35, v[98:99], s[8:9] offset:3584
	s_add_i32 s13, s13, 0x800
	s_cmp_ge_u32 s13, 0x2400
	s_cbranch_scc1 .Ln0_done
; DI unsigned pk_bf16(float lo, float hi) { f32x2 v = {lo, hi}; hbf16x2 r = __builtin_convertvector(v, hbf16x2); return __builtin_bit_cast(unsigned, r); }
; DI void norm_mod_store(const f32x4 (&v)[8], const float* gain, const float* shift, const float* scale, bf16_t* hrow, int lane, unsigned char* h8row = nullptr) {
;     float ss = 0.f;
; #pragma unroll
;     for (int i = 0; i < 8; ++i) ss += v[i][0] * v[i][0] + v[i][1] * v[i][1] + v[i][2] * v[i][2] + v[i][3] * v[i][3];
;     ss = wave_sum(ss);
;     const float r = rsqrtf(ss * (1.0f / DM) + EPS);
; #pragma unroll
;     for (int i = 0; i < 8; ++i) {
;         const int col = 4 * lane + 256 * i;
;         const f32x4 g = *(const f32x4*)(gain + col), sh = *(const f32x4*)(shift + col), sc = *(const f32x4*)(scale + col);
;         const f32x4 h = (v[i] * r * g) * (1.0f + sc) + sh;
;         if (h8row) *(unsigned*)(h8row + col) = pk_fp8x4(h[0], h[1], h[2], h[3]);
;         else { u32x2 w; w.x = pk_bf16(h[0], h[1]); w.y = pk_bf16(h[2], h[3]); *(u32x2*)(hrow + col) = w; }
;     }
; DI void phase_norm0(const Params& p, int G, int bid) {
;     ...
;     for (int row = bid * 8 + wave; row < NTOK; row += G * 8) {
;         const float* xr = row < NCTX ? p.in[2] + (size_t)row * DM : p.in[0] + (size_t)(row - NCTX) * DM;
;         f32x4 v[8];
; #pragma unroll
;         for (int i = 0; i < 8; ++i) v[i] = *(const f32x4*)(xr + 4 * lane + 256 * i);
;         const float* md = MOD + (size_t)row_mod(row) * MODN;
;         norm_mod_store(v, p.in[9], md, md + DM, H + (size_t)row * DM, lane);
;     }
	s_sub_i32 s15, s13, 0x400
	s_lshr_b32 s15, s15, 11
	s_cmp_lt_u32 s13, 0x400
	s_cselect_b32 s15, 4, s15
	s_mul_i32 s15, s15, 0xc000
	s_add_u32 s4, s50, s15
	s_addc_u32 s5, s51, 0
	s_add_u32 s4, s4, 0x10000
	s_addc_u32 s5, s5, 0
	s_add_u32 s6, s4, 0x2000
	s_addc_u32 s7, s5, 0
	s_lshl_b32 s15, s13, 12
	s_add_u32 s8, s50, s15
	s_addc_u32 s9, s51, 0
	s_add_u32 s8, s8, 0x2420e000
	s_addc_u32 s9, s9, 0
	global_load_dwordx4 v[142:145], v1, s[4:5] offset:0
	global_load_dwordx4 v[174:177], v1, s[6:7] offset:0
	global_load_dwordx4 v[146:149], v1, s[4:5] offset:1024
	global_load_dwordx4 v[178:181], v1, s[6:7] offset:1024
	global_load_dwordx4 v[150:153], v1, s[4:5] offset:2048
	global_load_dwordx4 v[182:185], v1, s[6:7] offset:2048
	global_load_dwordx4 v[154:157], v1, s[4:5] offset:3072
	global_load_dwordx4 v[186:189], v1, s[6:7] offset:3072
	global_load_dwordx4 v[158:161], v34, s[4:5] offset:0
	global_load_dwordx4 v[190:193], v34, s[6:7] offset:0
	global_load_dwordx4 v[162:165], v34, s[4:5] offset:1024
	global_load_dwordx4 v[194:197], v34, s[6:7] offset:1024
	global_load_dwordx4 v[166:169], v34, s[4:5] offset:2048
	global_load_dwordx4 v[198:201], v34, s[6:7] offset:2048
	global_load_dwordx4 v[170:173], v34, s[4:5] offset:3072
	global_load_dwordx4 v[202:205], v34, s[6:7] offset:3072
	s_add_i32 s16, s13, 0x800
	s_cmp_ge_u32 s16, 0x2400
	s_cselect_b32 s16, s13, s16
	s_sub_i32 s15, s16, 0x400
	s_cmp_lt_u32 s16, 0x400
	s_cselect_b32 s15, s16, s15
	s_cselect_b32 s2, s56, s52
	s_cselect_b32 s3, s57, s53
	s_lshl_b32 s15, s15, 13
	s_add_u32 s2, s2, s15
	s_addc_u32 s3, s3, 0
	global_load_dwordx4 v[40:43], v1, s[2:3] offset:0 nt
	global_load_dwordx4 v[44:47], v1, s[2:3] offset:1024 nt
	global_load_dwordx4 v[48:51], v1, s[2:3] offset:2048 nt
	global_load_dwordx4 v[52:55], v1, s[2:3] offset:3072 nt
	global_load_dwordx4 v[56:59], v34, s[2:3] offset:0 nt
	global_load_dwordx4 v[60:63], v34, s[2:3] offset:1024 nt
	global_load_dwordx4 v[64:67], v34, s[2:3] offset:2048 nt
	global_load_dwordx4 v[68:71], v34, s[2:3] offset:3072 nt
	s_waitcnt vmcnt(32)
	v_mul_f32_e32 v80, v3, v3
	v_fmac_f32_e32 v80, v2, v2
	v_fmac_f32_e32 v80, v4, v4
	v_fmac_f32_e32 v80, v5, v5
	v_mul_f32_e32 v82, v7, v7
	v_fmac_f32_e32 v82, v6, v6
	v_fmac_f32_e32 v82, v8, v8
	v_fmac_f32_e32 v82, v9, v9
	v_add_f32_e32 v80, v80, v82
	v_mul_f32_e32 v82, v11, v11
	v_fmac_f32_e32 v82, v10, v10
	v_fmac_f32_e32 v82, v12, v12
	v_fmac_f32_e32 v82, v13, v13
	v_add_f32_e32 v80, v80, v82
	v_mul_f32_e32 v82, v15, v15
	v_fmac_f32_e32 v82, v14, v14
	v_fmac_f32_e32 v82, v16, v16
	v_fmac_f32_e32 v82, v17, v17
	v_add_f32_e32 v80, v80, v82
	v_mul_f32_e32 v82, v19, v19
	v_fmac_f32_e32 v82, v18, v18
	v_fmac_f32_e32 v82, v20, v20
	v_fmac_f32_e32 v82, v21, v21
	v_add_f32_e32 v80, v80, v82
	v_mul_f32_e32 v82, v23, v23
	v_fmac_f32_e32 v82, v22, v22
	v_fmac_f32_e32 v82, v24, v24
	v_fmac_f32_e32 v82, v25, v25
	v_add_f32_e32 v80, v80, v82
	v_mul_f32_e32 v82, v27, v27
	v_fmac_f32_e32 v82, v26, v26
	v_fmac_f32_e32 v82, v28, v28
	v_fmac_f32_e32 v82, v29, v29
	v_add_f32_e32 v80, v80, v82
	v_mul_f32_e32 v82, v31, v31
	v_fmac_f32_e32 v82, v30, v30
	v_fmac_f32_e32 v82, v32, v32
	v_fmac_f32_e32 v82, v33, v33
	v_add_f32_e32 v80, v80, v82
	ds_bpermute_b32 v82, v72, v80
	s_waitcnt lgkmcnt(0)
	v_add_f32_e32 v80, v80, v82
	ds_bpermute_b32 v82, v73, v80
	s_waitcnt lgkmcnt(0)
	v_add_f32_e32 v80, v80, v82
	ds_bpermute_b32 v82, v74, v80
	s_waitcnt lgkmcnt(0)
	v_add_f32_e32 v80, v80, v82
	ds_bpermute_b32 v82, v75, v80
	s_waitcnt lgkmcnt(0)
	v_add_f32_e32 v80, v80, v82
	ds_bpermute_b32 v82, v76, v80
	s_waitcnt lgkmcnt(0)
	v_add_f32_e32 v80, v80, v82
	ds_bpermute_b32 v82, v77, v80
	s_waitcnt lgkmcnt(0)
	v_add_f32_e32 v80, v80, v82
	v_mov_b32_e32 v83, 0x358637bd
	v_fmamk_f32 v80, v80, 0x3a000000, v83
	v_cmp_gt_f32_e32 vcc, 0x800000, v80
	v_mul_f32_e32 v82, 0x4b800000, v80
	s_nop 1
	v_cndmask_b32_e32 v80, v80, v82, vcc
	v_rsq_f32_e32 v80, v80
	s_nop 0
	v_mul_f32_e32 v82, 0x45800000, v80
	s_nop 0
	v_cndmask_b32_e32 v80, v80, v82, vcc
	s_waitcnt vmcnt(22)
	v_pk_mul_f32 v[2:3], v[2:3], v[80:81] op_sel_hi:[1,0]
	v_pk_mul_f32 v[4:5], v[4:5], v[80:81] op_sel_hi:[1,0]
	v_pk_add_f32 v[174:175], v[174:175], 1.0 op_sel_hi:[1,0]
	v_pk_add_f32 v[176:177], v[176:177], 1.0 op_sel_hi:[1,0]
	v_pk_mul_f32 v[2:3], v[110:111], v[2:3]
	v_pk_mul_f32 v[4:5], v[112:113], v[4:5]
	v_pk_fma_f32 v[2:3], v[174:175], v[2:3], v[142:143]
	v_pk_fma_f32 v[4:5], v[176:177], v[4:5], v[144:145]
	v_cvt_pk_bf16_f32 v84, v2, v3
	v_cvt_pk_bf16_f32 v85, v4, v5
	global_store_dwordx2 v35, v[84:85], s[8:9] offset:0
	s_waitcnt vmcnt(21)
	v_pk_mul_f32 v[6:7], v[6:7], v[80:81] op_sel_hi:[1,0]
	v_pk_mul_f32 v[8:9], v[8:9], v[80:81] op_sel_hi:[1,0]
	v_pk_add_f32 v[178:179], v[178:179], 1.0 op_sel_hi:[1,0]
	v_pk_add_f32 v[180:181], v[180:181], 1.0 op_sel_hi:[1,0]
	v_pk_mul_f32 v[6:7], v[114:115], v[6:7]
	v_pk_mul_f32 v[8:9], v[116:117], v[8:9]
	v_pk_fma_f32 v[6:7], v[178:179], v[6:7], v[146:147]
	v_pk_fma_f32 v[8:9], v[180:181], v[8:9], v[148:149]
	v_cvt_pk_bf16_f32 v86, v6, v7
	v_cvt_pk_bf16_f32 v87, v8, v9
	global_store_dwordx2 v35, v[86:87], s[8:9] offset:512
	s_waitcnt vmcnt(20)
	v_pk_mul_f32 v[10:11], v[10:11], v[80:81] op_sel_hi:[1,0]
	v_pk_mul_f32 v[12:13], v[12:13], v[80:81] op_sel_hi:[1,0]
	v_pk_add_f32 v[182:183], v[182:183], 1.0 op_sel_hi:[1,0]
	v_pk_add_f32 v[184:185], v[184:185], 1.0 op_sel_hi:[1,0]
	v_pk_mul_f32 v[10:11], v[118:119], v[10:11]
	v_pk_mul_f32 v[12:13], v[120:121], v[12:13]
	v_pk_fma_f32 v[10:11], v[182:183], v[10:11], v[150:151]
	v_pk_fma_f32 v[12:13], v[184:185], v[12:13], v[152:153]
	v_cvt_pk_bf16_f32 v88, v10, v11
	v_cvt_pk_bf16_f32 v89, v12, v13
	global_store_dwordx2 v35, v[88:89], s[8:9] offset:1024
	s_waitcnt vmcnt(19)
; DI unsigned pk_bf16(float lo, float hi) { f32x2 v = {lo, hi}; hbf16x2 r = __builtin_convertvector(v, hbf16x2); return __builtin_bit_cast(unsigned, r); }
; DI void norm_mod_store(const f32x4 (&v)[8], const float* gain, const float* shift, const float* scale, bf16_t* hrow, int lane, unsigned char* h8row = nullptr) {
;     ...
;     const float r = rsqrtf(ss * (1.0f / DM) + EPS);
; #pragma unroll
;     for (int i = 0; i < 8; ++i) {
;         const int col = 4 * lane + 256 * i;
;         const f32x4 g = *(const f32x4*)(gain + col), sh = *(const f32x4*)(shift + col), sc = *(const f32x4*)(scale + col);
;         const f32x4 h = (v[i] * r * g) * (1.0f + sc) + sh;
;         if (h8row) *(unsigned*)(h8row + col) = pk_fp8x4(h[0], h[1], h[2], h[3]);
;         else { u32x2 w; w.x = pk_bf16(h[0], h[1]); w.y = pk_bf16(h[2], h[3]); *(u32x2*)(hrow + col) = w; }
;     }
; DI void phase_norm0(const Params& p, int G, int bid) {
;     ...
;     for (int row = bid * 8 + wave; row < NTOK; row += G * 8) {
;         const float* xr = row < NCTX ? p.in[2] + (size_t)row * DM : p.in[0] + (size_t)(row - NCTX) * DM;
;         f32x4 v[8];
; #pragma unroll
;         for (int i = 0; i < 8; ++i) v[i] = *(const f32x4*)(xr + 4 * lane + 256 * i);
;         const float* md = MOD + (size_t)row_mod(row) * MODN;
;         norm_mod_store(v, p.in[9], md, md + DM, H + (size_t)row * DM, lane);
;     }
	v_pk_mul_f32 v[14:15], v[14:15], v[80:81] op_sel_hi:[1,0]
	v_pk_mul_f32 v[16:17], v[16:17], v[80:81] op_sel_hi:[1,0]
	v_pk_add_f32 v[186:187], v[186:187], 1.0 op_sel_hi:[1,0]
	v_pk_add_f32 v[188:189], v[188:189], 1.0 op_sel_hi:[1,0]
	v_pk_mul_f32 v[14:15], v[122:123], v[14:15]
	v_pk_mul_f32 v[16:17], v[124:125], v[16:17]
	v_pk_fma_f32 v[14:15], v[186:187], v[14:15], v[154:155]
	v_pk_fma_f32 v[16:17], v[188:189], v[16:17], v[156:157]
	v_cvt_pk_bf16_f32 v90, v14, v15
	v_cvt_pk_bf16_f32 v91, v16, v17
	global_store_dwordx2 v35, v[90:91], s[8:9] offset:1536
	s_waitcnt vmcnt(18)
	v_pk_mul_f32 v[18:19], v[18:19], v[80:81] op_sel_hi:[1,0]
	v_pk_mul_f32 v[20:21], v[20:21], v[80:81] op_sel_hi:[1,0]
	v_pk_add_f32 v[190:191], v[190:191], 1.0 op_sel_hi:[1,0]
	v_pk_add_f32 v[192:193], v[192:193], 1.0 op_sel_hi:[1,0]
	v_pk_mul_f32 v[18:19], v[126:127], v[18:19]
	v_pk_mul_f32 v[20:21], v[128:129], v[20:21]
	v_pk_fma_f32 v[18:19], v[190:191], v[18:19], v[158:159]
	v_pk_fma_f32 v[20:21], v[192:193], v[20:21], v[160:161]
	v_cvt_pk_bf16_f32 v92, v18, v19
	v_cvt_pk_bf16_f32 v93, v20, v21
	global_store_dwordx2 v35, v[92:93], s[8:9] offset:2048
	s_waitcnt vmcnt(17)
	v_pk_mul_f32 v[22:23], v[22:23], v[80:81] op_sel_hi:[1,0]
	v_pk_mul_f32 v[24:25], v[24:25], v[80:81] op_sel_hi:[1,0]
	v_pk_add_f32 v[194:195], v[194:195], 1.0 op_sel_hi:[1,0]
	v_pk_add_f32 v[196:197], v[196:197], 1.0 op_sel_hi:[1,0]
	v_pk_mul_f32 v[22:23], v[130:131], v[22:23]
	v_pk_mul_f32 v[24:25], v[132:133], v[24:25]
	v_pk_fma_f32 v[22:23], v[194:195], v[22:23], v[162:163]
	v_pk_fma_f32 v[24:25], v[196:197], v[24:25], v[164:165]
	v_cvt_pk_bf16_f32 v94, v22, v23
	v_cvt_pk_bf16_f32 v95, v24, v25
	global_store_dwordx2 v35, v[94:95], s[8:9] offset:2560
	s_waitcnt vmcnt(16)
	v_pk_mul_f32 v[26:27], v[26:27], v[80:81] op_sel_hi:[1,0]
	v_pk_mul_f32 v[28:29], v[28:29], v[80:81] op_sel_hi:[1,0]
	v_pk_add_f32 v[198:199], v[198:199], 1.0 op_sel_hi:[1,0]
	v_pk_add_f32 v[200:201], v[200:201], 1.0 op_sel_hi:[1,0]
	v_pk_mul_f32 v[26:27], v[134:135], v[26:27]
	v_pk_mul_f32 v[28:29], v[136:137], v[28:29]
	v_pk_fma_f32 v[26:27], v[198:199], v[26:27], v[166:167]
	v_pk_fma_f32 v[28:29], v[200:201], v[28:29], v[168:169]
	v_cvt_pk_bf16_f32 v96, v26, v27
	v_cvt_pk_bf16_f32 v97, v28, v29
	global_store_dwordx2 v35, v[96:97], s[8:9] offset:3072
	s_waitcnt vmcnt(15)
	v_pk_mul_f32 v[30:31], v[30:31], v[80:81] op_sel_hi:[1,0]
	v_pk_mul_f32 v[32:33], v[32:33], v[80:81] op_sel_hi:[1,0]
	v_pk_add_f32 v[202:203], v[202:203], 1.0 op_sel_hi:[1,0]
	v_pk_add_f32 v[204:205], v[204:205], 1.0 op_sel_hi:[1,0]
	v_pk_mul_f32 v[30:31], v[138:139], v[30:31]
	v_pk_mul_f32 v[32:33], v[140:141], v[32:33]
	v_pk_fma_f32 v[30:31], v[202:203], v[30:31], v[170:171]
	v_pk_fma_f32 v[32:33], v[204:205], v[32:33], v[172:173]
	v_cvt_pk_bf16_f32 v98, v30, v31
	v_cvt_pk_bf16_f32 v99, v32, v33
	global_store_dwordx2 v35, v[98:99], s[8:9] offset:3584
	s_add_i32 s13, s13, 0x800
	s_cmp_ge_u32 s13, 0x2400
	s_cbranch_scc1 .Ln0_done
	s_sub_i32 s15, s13, 0x400
	s_lshr_b32 s15, s15, 11
	s_cmp_lt_u32 s13, 0x400
	s_cselect_b32 s15, 4, s15
	s_mul_i32 s15, s15, 0xc000
	s_add_u32 s4, s50, s15
	s_addc_u32 s5, s51, 0
	s_add_u32 s4, s4, 0x10000
	s_addc_u32 s5, s5, 0
	s_add_u32 s6, s4, 0x2000
	s_addc_u32 s7, s5, 0
	s_lshl_b32 s15, s13, 12
	s_add_u32 s8, s50, s15
	s_addc_u32 s9, s51, 0
	s_add_u32 s8, s8, 0x2420e000
	s_addc_u32 s9, s9, 0
	global_load_dwordx4 v[142:145], v1, s[4:5] offset:0
	global_load_dwordx4 v[174:177], v1, s[6:7] offset:0
	global_load_dwordx4 v[146:149], v1, s[4:5] offset:1024
	global_load_dwordx4 v[178:181], v1, s[6:7] offset:1024
	global_load_dwordx4 v[150:153], v1, s[4:5] offset:2048
	global_load_dwordx4 v[182:185], v1, s[6:7] offset:2048
	global_load_dwordx4 v[154:157], v1, s[4:5] offset:3072
	global_load_dwordx4 v[186:189], v1, s[6:7] offset:3072
	global_load_dwordx4 v[158:161], v34, s[4:5] offset:0
	global_load_dwordx4 v[190:193], v34, s[6:7] offset:0
	global_load_dwordx4 v[162:165], v34, s[4:5] offset:1024
	global_load_dwordx4 v[194:197], v34, s[6:7] offset:1024
	global_load_dwordx4 v[166:169], v34, s[4:5] offset:2048
	global_load_dwordx4 v[198:201], v34, s[6:7] offset:2048
	global_load_dwordx4 v[170:173], v34, s[4:5] offset:3072
	global_load_dwordx4 v[202:205], v34, s[6:7] offset:3072
	s_waitcnt vmcnt(24)
	v_mul_f32_e32 v80, v41, v41
	v_fmac_f32_e32 v80, v40, v40
	v_fmac_f32_e32 v80, v42, v42
	v_fmac_f32_e32 v80, v43, v43
	v_mul_f32_e32 v82, v45, v45
	v_fmac_f32_e32 v82, v44, v44
	v_fmac_f32_e32 v82, v46, v46
	v_fmac_f32_e32 v82, v47, v47
	v_add_f32_e32 v80, v80, v82
	v_mul_f32_e32 v82, v49, v49
	v_fmac_f32_e32 v82, v48, v48
	v_fmac_f32_e32 v82, v50, v50
	v_fmac_f32_e32 v82, v51, v51
	v_add_f32_e32 v80, v80, v82
	v_mul_f32_e32 v82, v53, v53
	v_fmac_f32_e32 v82, v52, v52
	v_fmac_f32_e32 v82, v54, v54
	v_fmac_f32_e32 v82, v55, v55
	v_add_f32_e32 v80, v80, v82
	v_mul_f32_e32 v82, v57, v57
	v_fmac_f32_e32 v82, v56, v56
	v_fmac_f32_e32 v82, v58, v58
	v_fmac_f32_e32 v82, v59, v59
	v_add_f32_e32 v80, v80, v82
	v_mul_f32_e32 v82, v61, v61
	v_fmac_f32_e32 v82, v60, v60
	v_fmac_f32_e32 v82, v62, v62
	v_fmac_f32_e32 v82, v63, v63
	v_add_f32_e32 v80, v80, v82
	v_mul_f32_e32 v82, v65, v65
	v_fmac_f32_e32 v82, v64, v64
	v_fmac_f32_e32 v82, v66, v66
	v_fmac_f32_e32 v82, v67, v67
	v_add_f32_e32 v80, v80, v82
	v_mul_f32_e32 v82, v69, v69
	v_fmac_f32_e32 v82, v68, v68
	v_fmac_f32_e32 v82, v70, v70
	v_fmac_f32_e32 v82, v71, v71
	v_add_f32_e32 v80, v80, v82
	ds_bpermute_b32 v82, v72, v80
	s_waitcnt lgkmcnt(0)
	v_add_f32_e32 v80, v80, v82
	ds_bpermute_b32 v82, v73, v80
	s_waitcnt lgkmcnt(0)
	v_add_f32_e32 v80, v80, v82
	ds_bpermute_b32 v82, v74, v80
	s_waitcnt lgkmcnt(0)
; DI unsigned pk_bf16(float lo, float hi) { f32x2 v = {lo, hi}; hbf16x2 r = __builtin_convertvector(v, hbf16x2); return __builtin_bit_cast(unsigned, r); }
; __device__ __forceinline__ unsigned xb_add(unsigned* p, unsigned v) { return __hip_atomic_fetch_add(p, v, __ATOMIC_RELAXED, __HIP_MEMORY_SCOPE_AGENT); }
; __device__ __forceinline__ void xcd_barrier(const XcdBarrier& b) {
;     asm volatile("s_waitcnt vmcnt(0)" ::: "memory");
;     __syncthreads();
;     if (threadIdx.x == 0) {
;         unsigned* bar = b.bar;
;         __builtin_amdgcn_s_waitcnt(0);
;         unsigned nloc = b.st[0], nx = b.st[1];
;         if (nloc == 0u) { xcd_barrier_complete(bar, b.x, nloc, nx); b.st[0] = nloc; b.st[1] = nx; }
;         const unsigned old = xb_add(&bar[XB_XSUB(b.x)], 1u);
; DI void norm_mod_store(const f32x4 (&v)[8], const float* gain, const float* shift, const float* scale, bf16_t* hrow, int lane, unsigned char* h8row = nullptr) {
;     ...
;     const float r = rsqrtf(ss * (1.0f / DM) + EPS);
; #pragma unroll
;     for (int i = 0; i < 8; ++i) {
;         const int col = 4 * lane + 256 * i;
;         const f32x4 g = *(const f32x4*)(gain + col), sh = *(const f32x4*)(shift + col), sc = *(const f32x4*)(scale + col);
;         const f32x4 h = (v[i] * r * g) * (1.0f + sc) + sh;
;         if (h8row) *(unsigned*)(h8row + col) = pk_fp8x4(h[0], h[1], h[2], h[3]);
;         else { u32x2 w; w.x = pk_bf16(h[0], h[1]); w.y = pk_bf16(h[2], h[3]); *(u32x2*)(hrow + col) = w; }
;     }
	v_add_f32_e32 v80, v80, v82
	ds_bpermute_b32 v82, v75, v80
	s_waitcnt lgkmcnt(0)
	v_add_f32_e32 v80, v80, v82
	ds_bpermute_b32 v82, v76, v80
	s_waitcnt lgkmcnt(0)
	v_add_f32_e32 v80, v80, v82
	ds_bpermute_b32 v82, v77, v80
	s_waitcnt lgkmcnt(0)
	v_add_f32_e32 v80, v80, v82
	v_mov_b32_e32 v83, 0x358637bd
	v_fmamk_f32 v80, v80, 0x3a000000, v83
	v_cmp_gt_f32_e32 vcc, 0x800000, v80
	v_mul_f32_e32 v82, 0x4b800000, v80
	s_nop 1
	v_cndmask_b32_e32 v80, v80, v82, vcc
	v_rsq_f32_e32 v80, v80
	s_nop 0
	v_mul_f32_e32 v82, 0x45800000, v80
	s_nop 0
	v_cndmask_b32_e32 v80, v80, v82, vcc
	s_waitcnt vmcnt(14)
	v_pk_mul_f32 v[40:41], v[40:41], v[80:81] op_sel_hi:[1,0]
	v_pk_mul_f32 v[42:43], v[42:43], v[80:81] op_sel_hi:[1,0]
	v_pk_add_f32 v[174:175], v[174:175], 1.0 op_sel_hi:[1,0]
	v_pk_add_f32 v[176:177], v[176:177], 1.0 op_sel_hi:[1,0]
	v_pk_mul_f32 v[40:41], v[110:111], v[40:41]
	v_pk_mul_f32 v[42:43], v[112:113], v[42:43]
	v_pk_fma_f32 v[40:41], v[174:175], v[40:41], v[142:143]
	v_pk_fma_f32 v[42:43], v[176:177], v[42:43], v[144:145]
	v_cvt_pk_bf16_f32 v84, v40, v41
	v_cvt_pk_bf16_f32 v85, v42, v43
	global_store_dwordx2 v35, v[84:85], s[8:9] offset:0
	s_waitcnt vmcnt(13)
	v_pk_mul_f32 v[44:45], v[44:45], v[80:81] op_sel_hi:[1,0]
	v_pk_mul_f32 v[46:47], v[46:47], v[80:81] op_sel_hi:[1,0]
	v_pk_add_f32 v[178:179], v[178:179], 1.0 op_sel_hi:[1,0]
	v_pk_add_f32 v[180:181], v[180:181], 1.0 op_sel_hi:[1,0]
	v_pk_mul_f32 v[44:45], v[114:115], v[44:45]
	v_pk_mul_f32 v[46:47], v[116:117], v[46:47]
	v_pk_fma_f32 v[44:45], v[178:179], v[44:45], v[146:147]
	v_pk_fma_f32 v[46:47], v[180:181], v[46:47], v[148:149]
	v_cvt_pk_bf16_f32 v86, v44, v45
	v_cvt_pk_bf16_f32 v87, v46, v47
	global_store_dwordx2 v35, v[86:87], s[8:9] offset:512
	s_waitcnt vmcnt(12)
	v_pk_mul_f32 v[48:49], v[48:49], v[80:81] op_sel_hi:[1,0]
	v_pk_mul_f32 v[50:51], v[50:51], v[80:81] op_sel_hi:[1,0]
	v_pk_add_f32 v[182:183], v[182:183], 1.0 op_sel_hi:[1,0]
	v_pk_add_f32 v[184:185], v[184:185], 1.0 op_sel_hi:[1,0]
	v_pk_mul_f32 v[48:49], v[118:119], v[48:49]
	v_pk_mul_f32 v[50:51], v[120:121], v[50:51]
	v_pk_fma_f32 v[48:49], v[182:183], v[48:49], v[150:151]
	v_pk_fma_f32 v[50:51], v[184:185], v[50:51], v[152:153]
	v_cvt_pk_bf16_f32 v88, v48, v49
	v_cvt_pk_bf16_f32 v89, v50, v51
	global_store_dwordx2 v35, v[88:89], s[8:9] offset:1024
	s_waitcnt vmcnt(11)
	v_pk_mul_f32 v[52:53], v[52:53], v[80:81] op_sel_hi:[1,0]
	v_pk_mul_f32 v[54:55], v[54:55], v[80:81] op_sel_hi:[1,0]
	v_pk_add_f32 v[186:187], v[186:187], 1.0 op_sel_hi:[1,0]
	v_pk_add_f32 v[188:189], v[188:189], 1.0 op_sel_hi:[1,0]
	v_pk_mul_f32 v[52:53], v[122:123], v[52:53]
	v_pk_mul_f32 v[54:55], v[124:125], v[54:55]
	v_pk_fma_f32 v[52:53], v[186:187], v[52:53], v[154:155]
	v_pk_fma_f32 v[54:55], v[188:189], v[54:55], v[156:157]
	v_cvt_pk_bf16_f32 v90, v52, v53
	v_cvt_pk_bf16_f32 v91, v54, v55
	global_store_dwordx2 v35, v[90:91], s[8:9] offset:1536
	s_waitcnt vmcnt(10)
	v_pk_mul_f32 v[56:57], v[56:57], v[80:81] op_sel_hi:[1,0]
	v_pk_mul_f32 v[58:59], v[58:59], v[80:81] op_sel_hi:[1,0]
	v_pk_add_f32 v[190:191], v[190:191], 1.0 op_sel_hi:[1,0]
	v_pk_add_f32 v[192:193], v[192:193], 1.0 op_sel_hi:[1,0]
	v_pk_mul_f32 v[56:57], v[126:127], v[56:57]
	v_pk_mul_f32 v[58:59], v[128:129], v[58:59]
	v_pk_fma_f32 v[56:57], v[190:191], v[56:57], v[158:159]
	v_pk_fma_f32 v[58:59], v[192:193], v[58:59], v[160:161]
	v_cvt_pk_bf16_f32 v92, v56, v57
	v_cvt_pk_bf16_f32 v93, v58, v59
	global_store_dwordx2 v35, v[92:93], s[8:9] offset:2048
	s_waitcnt vmcnt(9)
	v_pk_mul_f32 v[60:61], v[60:61], v[80:81] op_sel_hi:[1,0]
	v_pk_mul_f32 v[62:63], v[62:63], v[80:81] op_sel_hi:[1,0]
	v_pk_add_f32 v[194:195], v[194:195], 1.0 op_sel_hi:[1,0]
	v_pk_add_f32 v[196:197], v[196:197], 1.0 op_sel_hi:[1,0]
	v_pk_mul_f32 v[60:61], v[130:131], v[60:61]
	v_pk_mul_f32 v[62:63], v[132:133], v[62:63]
	v_pk_fma_f32 v[60:61], v[194:195], v[60:61], v[162:163]
	v_pk_fma_f32 v[62:63], v[196:197], v[62:63], v[164:165]
	v_cvt_pk_bf16_f32 v94, v60, v61
	v_cvt_pk_bf16_f32 v95, v62, v63
	global_store_dwordx2 v35, v[94:95], s[8:9] offset:2560
	s_waitcnt vmcnt(8)
	v_pk_mul_f32 v[64:65], v[64:65], v[80:81] op_sel_hi:[1,0]
	v_pk_mul_f32 v[66:67], v[66:67], v[80:81] op_sel_hi:[1,0]
	v_pk_add_f32 v[198:199], v[198:199], 1.0 op_sel_hi:[1,0]
	v_pk_add_f32 v[200:201], v[200:201], 1.0 op_sel_hi:[1,0]
	v_pk_mul_f32 v[64:65], v[134:135], v[64:65]
	v_pk_mul_f32 v[66:67], v[136:137], v[66:67]
	v_pk_fma_f32 v[64:65], v[198:199], v[64:65], v[166:167]
	v_pk_fma_f32 v[66:67], v[200:201], v[66:67], v[168:169]
	v_cvt_pk_bf16_f32 v96, v64, v65
	v_cvt_pk_bf16_f32 v97, v66, v67
	global_store_dwordx2 v35, v[96:97], s[8:9] offset:3072
	s_waitcnt vmcnt(7)
	v_pk_mul_f32 v[68:69], v[68:69], v[80:81] op_sel_hi:[1,0]
	v_pk_mul_f32 v[70:71], v[70:71], v[80:81] op_sel_hi:[1,0]
	v_pk_add_f32 v[202:203], v[202:203], 1.0 op_sel_hi:[1,0]
	v_pk_add_f32 v[204:205], v[204:205], 1.0 op_sel_hi:[1,0]
	v_pk_mul_f32 v[68:69], v[138:139], v[68:69]
	v_pk_mul_f32 v[70:71], v[140:141], v[70:71]
	v_pk_fma_f32 v[68:69], v[202:203], v[68:69], v[170:171]
	v_pk_fma_f32 v[70:71], v[204:205], v[70:71], v[172:173]
	v_cvt_pk_bf16_f32 v98, v68, v69
	v_cvt_pk_bf16_f32 v99, v70, v71
	global_store_dwordx2 v35, v[98:99], s[8:9] offset:3584
.Ln0_done:
.LBB0_165:
	s_or_b64 exec, exec, s[0:1]
	s_cmp_lt_u32 s25, 3
	s_cbranch_scc1 .LBB0_215
	s_waitcnt vmcnt(0)
	v_cmp_eq_u32_e32 vcc, 0, v0
	s_barrier
	s_and_saveexec_b64 s[0:1], vcc
	s_cbranch_execz .LBB0_214
	s_add_u32 s2, s50, 0x200
	s_addc_u32 s3, s51, 0
	s_add_i32 s4, 0, 0x22000
	v_mov_b32_e32 v1, s4
	s_waitcnt vmcnt(0) expcnt(0) lgkmcnt(0)
	ds_read_b32 v3, v1
	s_add_i32 s4, 0, 0x22004
	v_mov_b32_e32 v1, s4
	ds_read_b32 v1, v1
	s_waitcnt lgkmcnt(1)
	v_cmp_ne_u32_e32 vcc, 0, v3
	s_cbranch_vccnz .LBB0_182
	s_add_u32 s4, s50, 0x1000
	s_addc_u32 s5, s51, 0
	s_load_dwordx2 s[12:13], s[28:29], 0x4
	s_add_u32 s6, s50, 0x1100
	s_addc_u32 s7, s51, 0
	s_add_u32 s8, s50, 0x1200
	s_addc_u32 s9, s51, 0
	s_add_u32 s10, s50, 0x1300
	s_waitcnt lgkmcnt(0)
	s_mul_i32 s18, s12, s23
	s_addc_u32 s11, s51, 0
	s_mul_i32 s18, s18, s13
	s_mov_b32 s19, 1
	v_mov_b32_e32 v17, 0
	s_branch .LBB0_170

; template <int DQ>
; DI AtDma at_dma_init(int ld_bytes, int wave, int lane) {
;     AtDma d; d.rope = 0u;
;     constexpr int PPR = DQ / 8;
; #pragma unroll
;     for (int k = 0; k < DQ / 64; ++k) { const int L = (wave + 8 * k) * 64 + lane, r = L / PPR, pc = (L % PPR) ^ at_kf<DQ>(r);
;         if (DQ == 192 && pc >= 16) { d.ko[k] = (unsigned)(r * 128 + (pc - 16) * 16); d.rope |= 1u << k; } else d.ko[k] = (unsigned)(r * ld_bytes + pc * 16); }
;     if (DQ == 128) d.ko[2] = 0u;
; #pragma unroll
;     for (int k = 0; k < 2; ++k) { const int L = (wave + 8 * k) * 64 + lane, r = L >> 4, pc = (L & 15) ^ (2 * (r & 7)); d.vo[k] = (unsigned)(r * ld_bytes + pc * 16); }
;     return d;
; }
; DI void phase_attn0(const Params& p, LAS unsigned char* lds, int G, int bid) {
;     const int tid = threadIdx.x, lane = tid & 63, wave = __builtin_amdgcn_readfirstlane(tid >> 6), h = lane >> 5;
;     const bf16_t* Q0 = (const bf16_t*)(p.ws + WS_Q0);
;     bf16_t* Y = (bf16_t*)(p.ws + WS_Y);
;     const float c2 = 0.07216878364870322f * LOG2E;
;     const AtRd rd = at_rd_init<192>(lane);
;     const AtDma dm = at_dma_init<192>(4096, wave, lane);
.LBB0_530:
	s_cmp_gt_i32 s24, 5
	s_cselect_b64 s[0:1], -1, 0
	s_cmp_lt_i32 s25, 6
	s_cselect_b64 s[2:3], -1, 0
	s_or_b64 s[0:1], s[0:1], s[2:3]
	s_and_b64 vcc, exec, s[0:1]
	s_cbranch_vccnz .LBB0_622
	s_bitcmp1_b32 s26, 1
	s_cbranch_scc1 .LBB0_560
	v_readfirstlane_b32 s2, v0
	s_movk_i32 s0, 0xffc0
	s_nop 0
	v_mov_b32_e32 v1, s2
	v_bfi_b32 v2, s0, v1, v0
	s_mov_b32 s0, 0x2aaaaaab
	v_mul_hi_i32 v1, v2, s0
	v_lshrrev_b32_e32 v3, 31, v1
	v_ashrrev_i32_e32 v1, 2, v1
	v_add_u32_e32 v1, v1, v3
	v_mul_lo_u32 v3, v1, 24
	v_sub_u32_e32 v3, v2, v3
	v_lshrrev_b32_e32 v4, 1, v1
	v_bitop3_b32 v3, v4, v3, 7 bitop3:0x6c
	v_cmp_gt_i32_e32 vcc, 16, v3
	v_lshlrev_b32_e32 v3, 4, v3
	s_and_saveexec_b64 s[0:1], vcc
	s_xor_b64 s[0:1], exec, s[0:1]
	v_lshl_add_u32 v162, v1, 12, v3
	s_or_saveexec_b64 s[0:1], s[0:1]
	v_mov_b32_e32 v4, 0
	s_xor_b64 exec, exec, s[0:1]
	v_lshlrev_b32_e32 v1, 7, v1
	s_movk_i32 s3, 0xff00
	v_add3_u32 v162, v1, v3, s3
	v_mov_b32_e32 v4, 1
	s_or_b64 exec, exec, s[0:1]
	v_add_u32_e32 v5, 0x200, v2
	s_mov_b32 s0, 0x2aaaaaab
	v_mul_hi_i32 v1, v5, s0
	v_lshrrev_b32_e32 v3, 31, v1
	v_ashrrev_i32_e32 v1, 2, v1
	v_add_u32_e32 v1, v1, v3
	v_mul_lo_u32 v3, v1, 24
	v_sub_u32_e32 v3, v5, v3
	v_lshrrev_b32_e32 v6, 1, v1
	v_bitop3_b32 v3, v6, v3, 7 bitop3:0x6c
	v_cmp_gt_i32_e32 vcc, 16, v3
	v_lshlrev_b32_e32 v3, 4, v3
	s_and_saveexec_b64 s[0:1], vcc
	s_xor_b64 s[0:1], exec, s[0:1]
	v_lshl_add_u32 v164, v1, 12, v3
	s_andn2_saveexec_b64 s[0:1], s[0:1]
	v_lshlrev_b32_e32 v1, 7, v1
	s_movk_i32 s3, 0xff00
	v_add3_u32 v164, v1, v3, s3
	v_or_b32_e32 v4, 2, v4
	s_or_b64 exec, exec, s[0:1]
	v_add_u32_e32 v3, 0x400, v2
	s_mov_b32 s0, 0x2aaaaaab
	v_mul_hi_i32 v1, v3, s0
	v_lshrrev_b32_e32 v6, 31, v1
	v_ashrrev_i32_e32 v1, 2, v1
	v_add_u32_e32 v1, v1, v6
	v_mul_lo_u32 v6, v1, 24
	v_sub_u32_e32 v3, v3, v6
	v_lshrrev_b32_e32 v6, 1, v1
	v_bitop3_b32 v3, v6, v3, 7 bitop3:0x6c
	v_cmp_gt_i32_e32 vcc, 16, v3
	v_lshlrev_b32_e32 v6, 4, v3
	s_and_saveexec_b64 s[0:1], vcc
	s_xor_b64 s[0:1], exec, s[0:1]
	v_lshl_add_u32 v166, v1, 12, v6
	s_or_saveexec_b64 s[0:1], s[0:1]
	v_and_b32_e32 v3, 63, v0
	s_xor_b64 exec, exec, s[0:1]
	v_lshlrev_b32_e32 v1, 7, v1
	s_movk_i32 s3, 0xff00
	v_add3_u32 v166, v1, v6, s3
	v_or_b32_e32 v4, 4, v4
	s_or_b64 exec, exec, s[0:1]
	v_lshrrev_b32_e32 v6, 5, v3
	v_bfe_u32 v10, v0, 1, 3
	s_lshr_b32 s2, s2, 6
	v_bitop3_b32 v11, v6, v10, 2 bitop3:0x36
	s_add_u32 s0, s50, 0x2c5ae000
	v_lshrrev_b32_e32 v1, 1, v0
	v_lshlrev_b32_e32 v180, 4, v11
	v_bitop3_b32 v11, v6, v10, 4 bitop3:0x36
	v_bitop3_b32 v10, v6, v10, 6 bitop3:0x36
	s_addc_u32 s1, s51, 0
	v_bitop3_b32 v1, v6, v1, 7 bitop3:0x78
	v_lshlrev_b32_e32 v182, 4, v10
	v_bfe_u32 v10, v3, 2, 2
	v_lshlrev_b32_e32 v6, 2, v6
	s_add_u32 s8, s50, 0x304ae000
	v_lshrrev_b32_e32 v8, 2, v3
	v_lshrrev_b32_e32 v9, 4, v3
	v_lshlrev_b32_e32 v181, 4, v11
	v_bfe_u32 v3, v3, 4, 1
	v_or_b32_e32 v11, v6, v10
	s_addc_u32 s9, s51, 0
	v_bitop3_b32 v14, v6, v3, v10 bitop3:0x36
	v_bitop3_b32 v3, v3, v11, 4 bitop3:0x36
	s_lshr_b32 s4, s23, 31
	v_and_b32_e32 v7, 31, v0
	v_lshlrev_b32_e32 v183, 5, v14
	v_or_b32_e32 v14, 2, v9
	v_lshlrev_b32_e32 v185, 5, v3
	v_or_b32_e32 v3, 6, v9
	s_movk_i32 s3, 0x180
	s_add_i32 s4, s23, s4
	v_ashrrev_i32_e32 v2, 4, v2
	v_bitop3_b32 v14, v6, v14, v10 bitop3:0x36
	v_bitop3_b32 v3, v6, v3, v10 bitop3:0x36
	v_and_b32_e32 v9, 15, v0
	v_mad_u32_u24 v187, v7, s3, 0
	s_add_i32 s3, s23, s22
	s_ashr_i32 s4, s4, 1
	v_lshlrev_b32_e32 v10, 1, v2
	s_sub_i32 s10, s3, s4
	v_bitop3_b32 v10, v10, v9, 14 bitop3:0x6c
	v_lshlrev_b32_e32 v2, 12, v2
	s_add_u32 s12, s50, 0x2e0ae000
	v_lshl_or_b32 v168, v10, 4, v2
	v_ashrrev_i32_e32 v2, 4, v5
	s_addc_u32 s13, s51, 0
	v_lshlrev_b32_e32 v5, 1, v2
	s_add_u32 s14, s50, 0x2c48e000
	v_bitop3_b32 v5, v5, v9, 14 bitop3:0x6c
	v_lshlrev_b32_e32 v2, 12, v2
	s_addc_u32 s15, s51, 0
	v_lshl_or_b32 v170, v5, 4, v2
	v_lshl_or_b32 v189, s2, 5, v7
	s_lshl_b32 s2, s2, 10
	v_and_b32_e32 v2, 1, v4
	s_add_i32 s27, s2, 0
	v_cmp_eq_u32_e64 s[2:3], 0, v2
	v_and_b32_e32 v2, 2, v4
	s_abs_i32 s16, s23
	v_cmp_eq_u32_e64 s[4:5], 0, v2
	v_cvt_f32_u32_e32 v2, s16
	s_sub_i32 s18, 0, s16
	s_ashr_i32 s17, s10, 31
	s_abs_i32 s10, s10
	v_rcp_iflag_f32_e32 v2, v2
	v_lshlrev_b32_e32 v13, 3, v0
	v_lshlrev_b32_e32 v186, 5, v3
	v_lshrrev_b32_e32 v3, 2, v0
	v_mul_f32_e32 v2, 0x4f7ffffe, v2
	v_cvt_u32_f32_e32 v2, v2
	v_lshlrev_b32_e32 v12, 8, v11
	v_and_b32_e32 v13, 24, v13
	v_and_b32_e32 v6, 8, v3
	v_readfirstlane_b32 s19, v2
	s_mul_i32 s18, s18, s19
	s_mul_hi_u32 s18, s19, s18
	s_add_i32 s19, s19, s18
	s_mul_hi_u32 s18, s10, s19
	s_mul_i32 s18, s18, s16
	s_sub_i32 s10, s10, s18
	s_sub_i32 s18, s10, s16
	s_cmp_ge_u32 s10, s16
	s_cselect_b32 s10, s18, s10
	s_sub_i32 s18, s10, s16
	s_cmp_ge_u32 s10, s16
	s_cselect_b32 s10, s18, s10
	s_xor_b32 s10, s10, s17
	v_mov_b32_e32 v3, 0
	v_and_b32_e32 v8, 8, v8
	v_and_b32_e32 v4, 4, v4
	s_sub_i32 s34, s10, s17
	v_mbcnt_lo_u32_b32 v2, -1, 0
	v_lshlrev_b32_e32 v1, 4, v1
	v_lshlrev_b32_e32 v184, 5, v14
	s_mov_b32 s11, 0
	v_add3_u32 v188, 0, v12, v13
	v_add_u32_e32 v190, 0x400, v189
	v_mov_b32_e32 v163, v3
	v_mov_b32_e32 v165, v3
	v_cmp_eq_u32_e64 s[6:7], 0, v4
	v_mov_b32_e32 v167, v3
	v_mov_b32_e32 v169, v3
	v_mov_b32_e32 v171, v3
	s_addk_i32 s34, 0x100
	s_mov_b64 s[16:17], -1
	s_movk_i32 s35, 0xc00
	v_lshlrev_b32_e32 v172, 1, v6
	s_add_i32 s40, s27, 0x2000
	s_add_i32 s41, s27, 0x4000
	s_mov_b64 s[18:19], 0x100
	s_add_i32 s54, s27, 0x12000
	s_add_i32 s55, s27, 0x14000
	s_mov_b32 s58, 0x41000000
	v_lshlrev_b32_e32 v174, 1, v8
	v_mbcnt_hi_u32_b32 v191, -1, v2
	s_branch .LBB0_546

; #define LAS __attribute__((address_space(3)))
; DI unsigned pk_bf16(float lo, float hi) { f32x2 v = {lo, hi}; hbf16x2 r = __builtin_convertvector(v, hbf16x2); return __builtin_bit_cast(unsigned, r); }
; #define MFMA32(a, b, c) __builtin_amdgcn_mfma_f32_32x32x16_bf16((a), (b), (c), 0, 0, 0)
;     DI const char* vb(int j) const { return KV + (size_t)keyrow0(j) * 4096 + head * 512 + 256; }
;     DI const char* vb(int q) const { return Z + (size_t)keyrow0(q) * (L1IN * 2) + (1280 + kvh * 128) * 2; }
;     DI const char* vb(int j) const { return Z + (size_t)keyrow0(j) * (L1IN * 2) + (3584 + head * 128) * 2; }
; template <class BiasFn, bool PRE = false>
; DI void at_sm(f32x16& s0, f32x16& s1, f32x16 (&o)[4], float& m, float& l, const float c2, const BiasFn& bias, const int lane, bf16x8 (&pf)[4]) {
;     ...
; #pragma unroll
;     for (int i = 0; i < 16; ++i) { s0[i] = __builtin_amdgcn_exp2f(s0[i]); s1[i] = __builtin_amdgcn_exp2f(s1[i]); rs += s0[i] + s1[i]; }
;     l += rs;
;     u32x4 w;
;     w.x = pk_bf16(s0[0], s0[1]); w.y = pk_bf16(s0[2], s0[3]); w.z = pk_bf16(s0[4], s0[5]); w.w = pk_bf16(s0[6], s0[7]); pf[0] = __builtin_bit_cast(bf16x8, w);
;     w.x = pk_bf16(s0[8], s0[9]); w.y = pk_bf16(s0[10], s0[11]); w.z = pk_bf16(s0[12], s0[13]); w.w = pk_bf16(s0[14], s0[15]); pf[1] = __builtin_bit_cast(bf16x8, w);
;     w.x = pk_bf16(s1[0], s1[1]); w.y = pk_bf16(s1[2], s1[3]); w.z = pk_bf16(s1[4], s1[5]); w.w = pk_bf16(s1[6], s1[7]); pf[2] = __builtin_bit_cast(bf16x8, w);
;     w.x = pk_bf16(s1[8], s1[9]); w.y = pk_bf16(s1[10], s1[11]); w.z = pk_bf16(s1[12], s1[13]); w.w = pk_bf16(s1[14], s1[15]); pf[3] = __builtin_bit_cast(bf16x8, w);
; }
; DI void at_pv(const LAS unsigned char* vs, const AtRd& rd, const bf16x8 (&pf)[4], f32x16 (&o)[4]) {
;     const LAS unsigned char* vb = vs + rd.vbase;
; #pragma unroll
;     for (int ks = 0; ks < 4; ++ks)
; #pragma unroll
;         for (int t = 0; t < 4; ++t) {
;             const s16x4 lo = __builtin_amdgcn_ds_read_tr16_b64_v4i16((LAS s16x4*)(vb + (16 * ks) * 256 + rd.vo[t]));
;             const s16x4 hi = __builtin_amdgcn_ds_read_tr16_b64_v4i16((LAS s16x4*)(vb + (16 * ks + 8) * 256 + rd.vo[t]));
;             const bf16x8 vf = __builtin_shufflevector(lo, hi, 0, 1, 2, 3, 4, 5, 6, 7);
;             o[t] = MFMA32(vf, pf[ks], o[t]);
;         }
; }
.LBB0_549:
	v_exp_f32_e32 v8, v98
	v_exp_f32_e32 v118, v82
	v_exp_f32_e32 v2, v99
	v_exp_f32_e32 v16, v83
	v_exp_f32_e32 v119, v84
	v_add_f32_e32 v17, v118, v8
	v_exp_f32_e32 v98, v85
	v_pk_add_f32 v[4:5], v[16:17], v[2:3]
	v_exp_f32_e32 v17, v100
	v_pk_add_f32 v[6:7], v[4:5], v[4:5] op_sel_hi:[0,1]
	v_exp_f32_e32 v6, v101
	v_exp_f32_e32 v100, v87
	v_add_f32_e32 v99, v119, v17
	v_exp_f32_e32 v120, v90
	v_pk_add_f32 v[4:5], v[98:99], v[6:7]
	v_exp_f32_e32 v7, v102
	v_pk_add_f32 v[12:13], v[4:5], v[4:5] op_sel_hi:[0,1]
	v_exp_f32_e32 v99, v86
	v_exp_f32_e32 v12, v103
	v_exp_f32_e32 v102, v89
	v_exp_f32_e32 v122, v94
	v_add_f32_e32 v101, v99, v7
	v_pk_add_f32 v[4:5], v[100:101], v[12:13]
	v_exp_f32_e32 v13, v104
	v_pk_add_f32 v[14:15], v[4:5], v[4:5] op_sel_hi:[0,1]
	v_exp_f32_e32 v101, v88
	v_exp_f32_e32 v14, v105
	v_exp_f32_e32 v94, v95
	v_mov_b32_e32 v175, v3
	v_add_f32_e32 v103, v101, v13
	v_pk_add_f32 v[4:5], v[102:103], v[14:15]
	v_exp_f32_e32 v103, v106
	v_pk_add_f32 v[104:105], v[4:5], v[4:5] op_sel_hi:[0,1]
	v_exp_f32_e32 v104, v107
	v_exp_f32_e32 v106, v91
	v_add_f32_e32 v107, v120, v103
	s_add_i32 s66, s66, s23
	v_pk_add_f32 v[4:5], v[106:107], v[104:105]
	s_nop 0
	v_pk_add_f32 v[114:115], v[4:5], v[4:5] op_sel_hi:[0,1]
	v_exp_f32_e32 v105, v108
	v_exp_f32_e32 v107, v92
	v_exp_f32_e32 v114, v109
	v_exp_f32_e32 v108, v93
	v_cvt_pk_bf16_f32 v4, v8, v2
	v_add_f32_e32 v109, v107, v105
	v_lshl_add_u32 v2, s10, 14, v188
	v_add_u32_e32 v2, 0x6000, v2
	v_pk_add_f32 v[86:87], v[108:109], v[114:115]
	v_add_u32_e32 v109, v2, v183
	ds_read_b64_tr_b16 v[8:9], v109 offset:49152
	ds_read_b64_tr_b16 v[10:11], v109 offset:51200
	v_cvt_pk_bf16_f32 v5, v17, v6
	v_add_u32_e32 v17, v2, v184
	v_pk_add_f32 v[116:117], v[86:87], v[86:87] op_sel_hi:[0,1]
	v_exp_f32_e32 v115, v110
	v_cvt_pk_bf16_f32 v6, v7, v12
	v_cvt_pk_bf16_f32 v7, v13, v14
	ds_read_b64_tr_b16 v[12:13], v17 offset:49152
	ds_read_b64_tr_b16 v[14:15], v17 offset:51200
	ds_read_b64_tr_b16 v[82:83], v109 offset:53248
	ds_read_b64_tr_b16 v[84:85], v109 offset:55296
	v_exp_f32_e32 v116, v111
	v_add_u32_e32 v121, v2, v185
	v_add_u32_e32 v2, v2, v186
	s_waitcnt lgkmcnt(4)
	v_mfma_f32_32x32x16_bf16 v[66:81], v[8:11], v[4:7], v[66:81]
	ds_read_b64_tr_b16 v[8:9], v121 offset:49152
	ds_read_b64_tr_b16 v[10:11], v121 offset:51200
	ds_read_b64_tr_b16 v[86:87], v17 offset:53248
	ds_read_b64_tr_b16 v[88:89], v17 offset:55296
	v_add_f32_e32 v95, v122, v115
	v_pk_add_f32 v[110:111], v[94:95], v[116:117]
	v_exp_f32_e32 v95, v112
	v_pk_add_f32 v[110:111], v[110:111], v[110:111] op_sel_hi:[0,1]
	v_exp_f32_e32 v110, v113
	s_lshl_b32 s10, s67, 8
	s_waitcnt lgkmcnt(6)
	v_mfma_f32_32x32x16_bf16 v[50:65], v[12:15], v[4:7], v[50:65]
	ds_read_b64_tr_b16 v[12:13], v2 offset:49152
	ds_read_b64_tr_b16 v[14:15], v2 offset:51200
	ds_read_b64_tr_b16 v[90:91], v121 offset:53248
	ds_read_b64_tr_b16 v[92:93], v121 offset:55296
	s_cmp_ge_i32 s66, s59
	s_waitcnt lgkmcnt(6)
	v_mfma_f32_32x32x16_bf16 v[34:49], v[8:11], v[4:7], v[34:49]
	ds_read_b64_tr_b16 v[8:9], v2 offset:53248
	ds_read_b64_tr_b16 v[10:11], v2 offset:55296
	s_waitcnt lgkmcnt(4)
	v_mfma_f32_32x32x16_bf16 v[18:33], v[12:15], v[4:7], v[18:33]
	v_cvt_pk_bf16_f32 v4, v103, v104
	v_cvt_pk_bf16_f32 v5, v105, v114
	v_cvt_pk_bf16_f32 v6, v115, v116
	v_cvt_pk_bf16_f32 v7, v95, v110
	s_nop 1
	v_mfma_f32_32x32x16_bf16 v[66:81], v[82:85], v[4:7], v[66:81]
	v_mfma_f32_32x32x16_bf16 v[50:65], v[86:89], v[4:7], v[50:65]
	s_waitcnt lgkmcnt(2)
	v_mfma_f32_32x32x16_bf16 v[34:49], v[90:93], v[4:7], v[34:49]
	s_waitcnt lgkmcnt(0)
	v_mfma_f32_32x32x16_bf16 v[18:33], v[8:11], v[4:7], v[18:33]
	ds_read_b64_tr_b16 v[4:5], v109 offset:57344
	ds_read_b64_tr_b16 v[6:7], v109 offset:59392
	v_cvt_pk_bf16_f32 v8, v118, v16
	v_cvt_pk_bf16_f32 v9, v119, v98
	v_cvt_pk_bf16_f32 v10, v99, v100
	v_cvt_pk_bf16_f32 v11, v101, v102
	ds_read_b64_tr_b16 v[12:13], v109 offset:61440
	ds_read_b64_tr_b16 v[14:15], v109 offset:63488
	s_waitcnt lgkmcnt(2)
	v_mfma_f32_32x32x16_bf16 v[66:81], v[4:7], v[8:11], v[66:81]
	ds_read_b64_tr_b16 v[4:5], v17 offset:57344
	ds_read_b64_tr_b16 v[6:7], v17 offset:59392
	ds_read_b64_tr_b16 v[82:83], v17 offset:61440
	ds_read_b64_tr_b16 v[84:85], v17 offset:63488
	s_waitcnt lgkmcnt(2)
	v_mfma_f32_32x32x16_bf16 v[50:65], v[4:7], v[8:11], v[50:65]
	ds_read_b64_tr_b16 v[4:5], v121 offset:57344
	ds_read_b64_tr_b16 v[6:7], v121 offset:59392
	ds_read_b64_tr_b16 v[86:87], v121 offset:61440
	ds_read_b64_tr_b16 v[88:89], v121 offset:63488
	s_waitcnt lgkmcnt(2)
	v_mfma_f32_32x32x16_bf16 v[34:49], v[4:7], v[8:11], v[34:49]
	ds_read_b64_tr_b16 v[4:5], v2 offset:57344
	ds_read_b64_tr_b16 v[6:7], v2 offset:59392
	ds_read_b64_tr_b16 v[90:91], v2 offset:61440
	ds_read_b64_tr_b16 v[92:93], v2 offset:63488
	v_exp_f32_e32 v2, v96
	s_waitcnt vmcnt(0)
	s_waitcnt lgkmcnt(0)
	s_barrier
; DI unsigned pk_bf16(float lo, float hi) { f32x2 v = {lo, hi}; hbf16x2 r = __builtin_convertvector(v, hbf16x2); return __builtin_bit_cast(unsigned, r); }
; DI unsigned at_swap_lo(unsigned a, unsigned b, unsigned& bo) { const auto r = __builtin_amdgcn_permlane32_swap(a, b, false, false); bo = r[1]; return r[0]; }
; DI void attn_store(const f32x16 (&o)[4], float l, float extra, bf16_t* orow, int lane) {
;     const int h = lane >> 5;
;     const float lt = l + __shfl_xor(l, 32) + extra;
;     const float inv = 1.0f / lt;
; #pragma unroll
;     for (int t = 0; t < 4; ++t)
; #pragma unroll
;         for (int pr = 0; pr < 2; ++pr) {
;             const int ga = 8 * pr, gb = 8 * pr + 4;
;             unsigned ax = pk_bf16(o[t][ga] * inv, o[t][ga + 1] * inv), ay = pk_bf16(o[t][ga + 2] * inv, o[t][ga + 3] * inv);
;             unsigned bx = pk_bf16(o[t][gb] * inv, o[t][gb + 1] * inv), by = pk_bf16(o[t][gb + 2] * inv, o[t][gb + 3] * inv);
;             u32x4 w; unsigned t0, t1;
;             w.x = at_swap_lo(ax, bx, t0); w.y = at_swap_lo(ay, by, t1); w.z = t0; w.w = t1;
;             *(u32x4*)(orow + 32 * t + 8 * (2 * pr + h)) = w;
;         }
; }
	v_mfma_f32_32x32x16_bf16 v[18:33], v[4:7], v[8:11], v[18:33]
	v_exp_f32_e32 v8, v97
	v_cvt_pk_bf16_f32 v4, v120, v106
	v_cvt_pk_bf16_f32 v5, v107, v108
	v_cvt_pk_bf16_f32 v6, v122, v94
	v_cvt_pk_bf16_f32 v7, v2, v8
	v_add_f32_e32 v9, v2, v95
	v_pk_add_f32 v[8:9], v[8:9], v[110:111]
	v_mfma_f32_32x32x16_bf16 v[66:81], v[12:15], v[4:7], v[66:81]
	v_add_f32_e32 v2, v8, v9
	v_add_f32_e32 v2, v173, v2
	v_mfma_f32_32x32x16_bf16 v[50:65], v[82:85], v[4:7], v[50:65]
	v_mfma_f32_32x32x16_bf16 v[34:49], v[86:89], v[4:7], v[34:49]
	v_mfma_f32_32x32x16_bf16 v[18:33], v[90:93], v[4:7], v[18:33]
	v_and_b32_e32 v5, 64, v191
	v_xor_b32_e32 v4, 32, v191
	v_add_u32_e32 v5, 64, v5
	v_cmp_lt_i32_e32 vcc, v4, v5
	s_nop 1
	v_cndmask_b32_e32 v4, v191, v4, vcc
	v_lshlrev_b32_e32 v4, 2, v4
	ds_bpermute_b32 v6, v4, v2
	v_lshlrev_b64 v[4:5], 12, v[176:177]
	v_lshl_add_u64 v[4:5], s[8:9], 0, v[4:5]
	v_lshl_add_u64 v[8:9], v[4:5], 0, s[10:11]
	v_lshl_add_u64 v[8:9], v[8:9], 0, v[174:175]
	s_waitcnt lgkmcnt(0)
	v_add_f32_e32 v2, v2, v6
	v_add_f32_e32 v2, 0, v2
	v_div_scale_f32 v6, s[30:31], v2, v2, 1.0
	v_rcp_f32_e32 v7, v6
	s_nop 0
	v_fma_f32 v4, -v6, v7, 1.0
	v_fmac_f32_e32 v7, v4, v7
	v_div_scale_f32 v4, vcc, 1.0, v2, 1.0
	v_mul_f32_e32 v5, v4, v7
	v_fma_f32 v10, -v6, v5, v4
	v_fmac_f32_e32 v5, v10, v7
	v_fma_f32 v4, -v6, v5, v4
	v_div_fmas_f32 v4, v4, v7, v5
	v_div_fixup_f32 v2, v4, v2, 1.0
	v_pk_mul_f32 v[4:5], v[66:67], v[2:3] op_sel_hi:[1,0]
	v_pk_mul_f32 v[6:7], v[68:69], v[2:3] op_sel_hi:[1,0]
	v_cvt_pk_bf16_f32 v4, v4, v5
	v_cvt_pk_bf16_f32 v5, v6, v7
	v_pk_mul_f32 v[6:7], v[70:71], v[2:3] op_sel_hi:[1,0]
	v_pk_mul_f32 v[10:11], v[72:73], v[2:3] op_sel_hi:[1,0]
	v_cvt_pk_bf16_f32 v6, v6, v7
	v_cvt_pk_bf16_f32 v7, v10, v11
	s_nop 0
	v_permlane32_swap_b32_e32 v4, v6
	v_permlane32_swap_b32_e32 v5, v7
	global_store_dwordx4 v[8:9], v[4:7], off
	v_pk_mul_f32 v[10:11], v[80:81], v[2:3] op_sel_hi:[1,0]
	s_nop 0
	v_pk_mul_f32 v[4:5], v[74:75], v[2:3] op_sel_hi:[1,0]
	v_pk_mul_f32 v[6:7], v[76:77], v[2:3] op_sel_hi:[1,0]
	v_cvt_pk_bf16_f32 v4, v4, v5
	v_cvt_pk_bf16_f32 v5, v6, v7
	v_pk_mul_f32 v[6:7], v[78:79], v[2:3] op_sel_hi:[1,0]
	s_nop 0
	v_cvt_pk_bf16_f32 v6, v6, v7
	v_cvt_pk_bf16_f32 v7, v10, v11
	s_nop 0
	v_permlane32_swap_b32_e32 v4, v6
	v_permlane32_swap_b32_e32 v5, v7
	global_store_dwordx4 v[8:9], v[4:7], off offset:32
	v_pk_mul_f32 v[10:11], v[56:57], v[2:3] op_sel_hi:[1,0]
	s_nop 0
	v_pk_mul_f32 v[4:5], v[50:51], v[2:3] op_sel_hi:[1,0]
	v_pk_mul_f32 v[6:7], v[52:53], v[2:3] op_sel_hi:[1,0]
	v_cvt_pk_bf16_f32 v4, v4, v5
	v_cvt_pk_bf16_f32 v5, v6, v7
	v_pk_mul_f32 v[6:7], v[54:55], v[2:3] op_sel_hi:[1,0]
	s_nop 0
	v_cvt_pk_bf16_f32 v6, v6, v7
	v_cvt_pk_bf16_f32 v7, v10, v11
	s_nop 0
	v_permlane32_swap_b32_e32 v4, v6
	v_permlane32_swap_b32_e32 v5, v7
	global_store_dwordx4 v[8:9], v[4:7], off offset:64
	v_pk_mul_f32 v[10:11], v[64:65], v[2:3] op_sel_hi:[1,0]
	s_nop 0
	v_pk_mul_f32 v[4:5], v[58:59], v[2:3] op_sel_hi:[1,0]
	v_pk_mul_f32 v[6:7], v[60:61], v[2:3] op_sel_hi:[1,0]
	v_cvt_pk_bf16_f32 v4, v4, v5
	v_cvt_pk_bf16_f32 v5, v6, v7
	v_pk_mul_f32 v[6:7], v[62:63], v[2:3] op_sel_hi:[1,0]
	s_nop 0
	v_cvt_pk_bf16_f32 v6, v6, v7
	v_cvt_pk_bf16_f32 v7, v10, v11
	s_nop 0
	v_permlane32_swap_b32_e32 v4, v6
	v_permlane32_swap_b32_e32 v5, v7
	global_store_dwordx4 v[8:9], v[4:7], off offset:96
	v_pk_mul_f32 v[10:11], v[40:41], v[2:3] op_sel_hi:[1,0]
	s_nop 0
	v_pk_mul_f32 v[4:5], v[34:35], v[2:3] op_sel_hi:[1,0]
	v_pk_mul_f32 v[6:7], v[36:37], v[2:3] op_sel_hi:[1,0]
	v_cvt_pk_bf16_f32 v4, v4, v5
	v_cvt_pk_bf16_f32 v5, v6, v7
	v_pk_mul_f32 v[6:7], v[38:39], v[2:3] op_sel_hi:[1,0]
	s_nop 0
	v_cvt_pk_bf16_f32 v6, v6, v7
	v_cvt_pk_bf16_f32 v7, v10, v11
	s_nop 0
	v_permlane32_swap_b32_e32 v4, v6
	v_permlane32_swap_b32_e32 v5, v7
	global_store_dwordx4 v[8:9], v[4:7], off offset:128
	v_pk_mul_f32 v[10:11], v[48:49], v[2:3] op_sel_hi:[1,0]
	s_nop 0
	v_pk_mul_f32 v[4:5], v[42:43], v[2:3] op_sel_hi:[1,0]
	v_pk_mul_f32 v[6:7], v[44:45], v[2:3] op_sel_hi:[1,0]
	v_cvt_pk_bf16_f32 v4, v4, v5
	v_cvt_pk_bf16_f32 v5, v6, v7
	v_pk_mul_f32 v[6:7], v[46:47], v[2:3] op_sel_hi:[1,0]
	s_nop 0
	v_cvt_pk_bf16_f32 v6, v6, v7
	v_cvt_pk_bf16_f32 v7, v10, v11
	s_nop 0
	v_permlane32_swap_b32_e32 v4, v6
	v_permlane32_swap_b32_e32 v5, v7
	global_store_dwordx4 v[8:9], v[4:7], off offset:160
	v_pk_mul_f32 v[10:11], v[24:25], v[2:3] op_sel_hi:[1,0]
	s_nop 0
	v_pk_mul_f32 v[4:5], v[18:19], v[2:3] op_sel_hi:[1,0]
	v_pk_mul_f32 v[6:7], v[20:21], v[2:3] op_sel_hi:[1,0]
	v_cvt_pk_bf16_f32 v4, v4, v5
	v_cvt_pk_bf16_f32 v5, v6, v7
	v_pk_mul_f32 v[6:7], v[22:23], v[2:3] op_sel_hi:[1,0]
	s_nop 0
	v_cvt_pk_bf16_f32 v6, v6, v7
	v_cvt_pk_bf16_f32 v7, v10, v11
	s_nop 0
	v_permlane32_swap_b32_e32 v4, v6
	v_permlane32_swap_b32_e32 v5, v7
	global_store_dwordx4 v[8:9], v[4:7], off offset:192
	v_pk_mul_f32 v[10:11], v[32:33], v[2:3] op_sel_hi:[1,0]
	s_nop 0
	v_pk_mul_f32 v[4:5], v[26:27], v[2:3] op_sel_hi:[1,0]
	v_pk_mul_f32 v[6:7], v[28:29], v[2:3] op_sel_hi:[1,0]
	v_cvt_pk_bf16_f32 v4, v4, v5
	v_cvt_pk_bf16_f32 v5, v6, v7
	v_pk_mul_f32 v[6:7], v[30:31], v[2:3] op_sel_hi:[1,0]
	s_nop 0
	v_cvt_pk_bf16_f32 v6, v6, v7
	v_cvt_pk_bf16_f32 v7, v10, v11
	s_nop 0
	v_permlane32_swap_b32_e32 v4, v6
	v_permlane32_swap_b32_e32 v5, v7
	global_store_dwordx4 v[8:9], v[4:7], off offset:224
	s_cbranch_scc1 .LBB0_545

; #define LAS __attribute__((address_space(3)))
;     DI const char* kb(int j) const { return KV + (size_t)keyrow0(j) * 4096 + head * 512; }
;     DI const char* vb(int j) const { return KV + (size_t)keyrow0(j) * 4096 + head * 512 + 256; }
;     DI const char* rb(int j) const { return KR + (size_t)keyrow0(j) * 128; }
;     DI const char* kb(int q) const { return Z + (size_t)keyrow0(q) * (L1IN * 2) + (1024 + kvh * 128) * 2; }
;     DI const char* vb(int q) const { return Z + (size_t)keyrow0(q) * (L1IN * 2) + (1280 + kvh * 128) * 2; }
;     DI const char* kb(int j) const { return Z + (size_t)keyrow0(j) * (L1IN * 2) + (2560 + head * 128) * 2; }
;     DI const char* vb(int j) const { return Z + (size_t)keyrow0(j) * (L1IN * 2) + (3584 + head * 128) * 2; }
; template <int DQ, class Drv>
; DI void at_run3(LAS unsigned char* lds, const Drv& D, const int n, const AtRd& rd, const AtDma& dm, const bf16x8 (&qf)[DQ / 16], f32x16 (&o)[4], float& m, float& l, const float c2, const int lane, const int wave) {
;     __syncthreads();
;     at_dma_k<DQ>(lds, D.kb(0), D.rb(0), dm, wave); at_dma_v(lds + AT_KSLOT, D.vb(0), dm, wave);
;     if (n > 1) { at_dma_k<DQ>(lds + AT4_SLOT, D.kb(1), D.rb(1), dm, wave); at_dma_v(lds + AT4_SLOT + AT_KSLOT, D.vb(1), dm, wave);
;         if (DQ == 192) asm volatile("s_waitcnt vmcnt(5)" ::: "memory"); else asm volatile("s_waitcnt vmcnt(4)" ::: "memory"); }
;     else asm volatile("s_waitcnt vmcnt(0)" ::: "memory");
;     __syncthreads();
; DI void phase_attn0(const Params& p, LAS unsigned char* lds, int G, int bid) {
;     ...
;     for (int it = 0; it < 2; ++it)
;     for (int u = it == 0 ? bid : 256 + (bid + G - G / 2) % G; u < (it == 0 ? 256 : 256 + 32); u += G) {
;         MlaDrv T; T.KV = (const char*)(p.ws + WS_KV0); T.KR = (const char*)(p.ws + WS_KR);
;         int qrow, nt;
;         if (u < 256) { T.b = u >> 6; T.head = (u >> 3) & 7; nt = 36; qrow = NCTX + T.b * SEQ + (u & 7) * 256 + wave * 32 + (lane & 31); }
;         else { const int v = u - 256; T.b = v >> 3; T.head = v & 7; nt = 4; qrow = T.b * CTX + wave * 32 + (lane & 31); }
;         bf16x8 qf[12];
; #pragma unroll
;         for (int s = 0; s < 12; ++s) qf[s] = *(const bf16x8*)(Q0 + (size_t)qrow * 1536 + T.head * 192 + 16 * s + 8 * h);
.LBB0_554:
	s_and_b32 s67, s10, 7
	v_mov_b64_e32 v[4:5], s[0:1]
	v_mad_i64_i32 v[4:5], s[30:31], v176, s35, v[4:5]
	s_mul_i32 s10, s67, 0x180
	v_lshl_add_u64 v[4:5], v[4:5], 0, s[10:11]
	v_mov_b32_e32 v173, v3
	v_lshl_add_u64 v[4:5], v[4:5], 0, v[172:173]
	v_ashrrev_i32_e32 v179, 31, v178
	global_load_dwordx4 v[158:161], v[4:5], off
	global_load_dwordx4 v[154:157], v[4:5], off offset:32
	global_load_dwordx4 v[150:153], v[4:5], off offset:64
	global_load_dwordx4 v[146:149], v[4:5], off offset:96
	global_load_dwordx4 v[142:145], v[4:5], off offset:128
	global_load_dwordx4 v[138:141], v[4:5], off offset:160
	global_load_dwordx4 v[134:137], v[4:5], off offset:192
	global_load_dwordx4 v[130:133], v[4:5], off offset:224
	global_load_dwordx4 v[126:129], v[4:5], off offset:256
	global_load_dwordx4 v[122:125], v[4:5], off offset:288
	global_load_dwordx4 v[118:121], v[4:5], off offset:320
	global_load_dwordx4 v[114:117], v[4:5], off offset:352
	v_lshlrev_b64 v[4:5], 12, v[178:179]
	v_lshl_add_u64 v[4:5], s[12:13], 0, v[4:5]
	s_lshl_b32 s10, s67, 9
	v_lshlrev_b64 v[6:7], 7, v[178:179]
	v_lshl_add_u64 v[4:5], v[4:5], 0, s[10:11]
	v_lshl_add_u64 v[6:7], s[14:15], 0, v[6:7]
	v_cndmask_b32_e64 v9, v7, v5, s[2:3]
	v_cndmask_b32_e64 v8, v6, v4, s[2:3]
	s_mov_b32 m0, s27
	v_lshl_add_u64 v[8:9], v[8:9], 0, v[162:163]
	s_waitcnt vmcnt(0)
	s_barrier
	global_load_lds_dwordx4 v[8:9], off
	v_cndmask_b32_e64 v9, v7, v5, s[4:5]
	v_cndmask_b32_e64 v8, v6, v4, s[4:5]
	v_lshl_add_u64 v[8:9], v[8:9], 0, v[164:165]
	s_mov_b32 m0, s40
	v_cndmask_b32_e64 v7, v7, v5, s[6:7]
	v_cndmask_b32_e64 v6, v6, v4, s[6:7]
	global_load_lds_dwordx4 v[8:9], off
	v_lshl_add_u64 v[6:7], v[6:7], 0, v[166:167]
	s_mov_b32 m0, s41
	v_mov_b32_e32 v16, v3
	global_load_lds_dwordx4 v[6:7], off
	v_lshl_add_u64 v[6:7], v[4:5], 0, v[168:169]
	v_lshl_add_u64 v[6:7], v[6:7], 0, s[18:19]
	s_mov_b32 m0, s54
	v_lshl_add_u64 v[4:5], v[4:5], 0, v[170:171]
	global_load_lds_dwordx4 v[6:7], off
	v_lshl_add_u64 v[4:5], v[4:5], 0, s[18:19]
	s_mov_b32 m0, s55
	v_mov_b32_e32 v17, v3
	global_load_lds_dwordx4 v[4:5], off
	s_add_u32 s100, s12, s10
	s_addc_u32 s101, s13, 0
	v_add_u32_e32 v4, 64, v178
	v_ashrrev_i32_e32 v5, 31, v4
	v_lshlrev_b64 v[6:7], 12, v[4:5]
	v_lshlrev_b64 v[4:5], 7, v[4:5]
	v_lshl_add_u64 v[6:7], s[100:101], 0, v[6:7]
	v_lshl_add_u64 v[4:5], s[14:15], 0, v[4:5]
	v_cndmask_b32_e64 v9, v5, v7, s[2:3]
	v_cndmask_b32_e64 v8, v4, v6, s[2:3]
	v_lshl_add_u64 v[8:9], v[8:9], 0, v[162:163]
	s_add_i32 m0, s27, 0x6000
	s_nop 0
	global_load_lds_dwordx4 v[8:9], off
	v_cndmask_b32_e64 v9, v5, v7, s[4:5]
	v_cndmask_b32_e64 v8, v4, v6, s[4:5]
	v_lshl_add_u64 v[8:9], v[8:9], 0, v[164:165]
	s_add_i32 m0, s27, 0x8000
	v_cndmask_b32_e64 v5, v5, v7, s[6:7]
	v_cndmask_b32_e64 v4, v4, v6, s[6:7]
	global_load_lds_dwordx4 v[8:9], off
	v_lshl_add_u64 v[4:5], v[4:5], 0, v[166:167]
	s_add_i32 m0, s27, 0xa000
	s_nop 0
	global_load_lds_dwordx4 v[4:5], off
	v_lshl_add_u64 v[4:5], v[6:7], 0, v[168:169]
	s_add_i32 m0, s27, 0x16000
	v_lshl_add_u64 v[4:5], v[4:5], 0, s[18:19]
	global_load_lds_dwordx4 v[4:5], off
	v_lshl_add_u64 v[4:5], v[6:7], 0, v[170:171]
	s_add_i32 m0, s27, 0x18000
	v_lshl_add_u64 v[4:5], v[4:5], 0, s[18:19]
	global_load_lds_dwordx4 v[4:5], off
	s_mov_b32 s98, 0
	s_mov_b32 s99, 2
	s_waitcnt vmcnt(5)
	v_or_b32_e32 v175, 0x300, v2
	s_add_u32 s30, s12, s10
	v_mov_b32_e32 v2, v3
	v_mov_b32_e32 v4, v3
	v_mov_b32_e32 v5, v3
	v_mov_b32_e32 v6, v3
	v_mov_b32_e32 v7, v3
	v_mov_b32_e32 v8, v3
	v_mov_b32_e32 v9, v3
	v_mov_b32_e32 v10, v3
	v_mov_b32_e32 v11, v3
	v_mov_b32_e32 v12, v3
	v_mov_b32_e32 v13, v3
	v_mov_b32_e32 v14, v3
	v_mov_b32_e32 v15, v3
	v_mov_b64_e32 v[32:33], v[16:17]
	v_mov_b64_e32 v[48:49], v[16:17]
	v_mov_b64_e32 v[64:65], v[16:17]
	v_mov_b64_e32 v[80:81], v[16:17]
	v_ashrrev_i32_e32 v177, 31, v176
	s_addc_u32 s31, s13, 0
	s_add_i32 s10, s68, 1
	s_mov_b32 s68, 0
	v_mov_b32_e32 v173, 0
	v_mov_b32_e32 v179, 0xc1f00000
	s_mov_b32 s69, 64
	v_mov_b64_e32 v[30:31], v[14:15]
	v_mov_b64_e32 v[28:29], v[12:13]
	v_mov_b64_e32 v[26:27], v[10:11]
	v_mov_b64_e32 v[24:25], v[8:9]
	v_mov_b64_e32 v[22:23], v[6:7]
	v_mov_b64_e32 v[20:21], v[4:5]
	v_mov_b64_e32 v[18:19], v[2:3]
	v_mov_b64_e32 v[46:47], v[14:15]
	v_mov_b64_e32 v[44:45], v[12:13]
	v_mov_b64_e32 v[42:43], v[10:11]
	v_mov_b64_e32 v[40:41], v[8:9]
	v_mov_b64_e32 v[38:39], v[6:7]
	v_mov_b64_e32 v[36:37], v[4:5]
	v_mov_b64_e32 v[34:35], v[2:3]
	v_mov_b64_e32 v[62:63], v[14:15]
	v_mov_b64_e32 v[60:61], v[12:13]
	v_mov_b64_e32 v[58:59], v[10:11]
	v_mov_b64_e32 v[56:57], v[8:9]
	v_mov_b64_e32 v[54:55], v[6:7]
	v_mov_b64_e32 v[52:53], v[4:5]
	v_mov_b64_e32 v[50:51], v[2:3]
	v_mov_b64_e32 v[78:79], v[14:15]
	v_mov_b64_e32 v[76:77], v[12:13]
	v_mov_b64_e32 v[74:75], v[10:11]
	v_mov_b64_e32 v[72:73], v[8:9]
	v_mov_b64_e32 v[70:71], v[6:7]
	v_mov_b64_e32 v[68:69], v[4:5]
	v_mov_b64_e32 v[66:67], v[2:3]
	s_waitcnt vmcnt(5) lgkmcnt(0)
	s_barrier
	s_branch .LBB0_556
; #define LAS __attribute__((address_space(3)))
; DI unsigned pk_bf16(float lo, float hi) { f32x2 v = {lo, hi}; hbf16x2 r = __builtin_convertvector(v, hbf16x2); return __builtin_bit_cast(unsigned, r); }
; template <class BiasFn, bool PRE = false>
; DI void at_sm(f32x16& s0, f32x16& s1, f32x16 (&o)[4], float& m, float& l, const float c2, const BiasFn& bias, const int lane, bf16x8 (&pf)[4]) {
;     ...
; #pragma unroll
;     for (int i = 0; i < 16; ++i) { s0[i] = __builtin_amdgcn_exp2f(s0[i]); s1[i] = __builtin_amdgcn_exp2f(s1[i]); rs += s0[i] + s1[i]; }
;     l += rs;
;     u32x4 w;
;     w.x = pk_bf16(s0[0], s0[1]); w.y = pk_bf16(s0[2], s0[3]); w.z = pk_bf16(s0[4], s0[5]); w.w = pk_bf16(s0[6], s0[7]); pf[0] = __builtin_bit_cast(bf16x8, w);
;     w.x = pk_bf16(s0[8], s0[9]); w.y = pk_bf16(s0[10], s0[11]); w.z = pk_bf16(s0[12], s0[13]); w.w = pk_bf16(s0[14], s0[15]); pf[1] = __builtin_bit_cast(bf16x8, w);
;     w.x = pk_bf16(s1[0], s1[1]); w.y = pk_bf16(s1[2], s1[3]); w.z = pk_bf16(s1[4], s1[5]); w.w = pk_bf16(s1[6], s1[7]); pf[2] = __builtin_bit_cast(bf16x8, w);
;     w.x = pk_bf16(s1[8], s1[9]); w.y = pk_bf16(s1[10], s1[11]); w.z = pk_bf16(s1[12], s1[13]); w.w = pk_bf16(s1[14], s1[15]); pf[3] = __builtin_bit_cast(bf16x8, w);
; }
; DI void at_pv(const LAS unsigned char* vs, const AtRd& rd, const bf16x8 (&pf)[4], f32x16 (&o)[4]) {
;     const LAS unsigned char* vb = vs + rd.vbase;
; #pragma unroll
;     for (int ks = 0; ks < 4; ++ks)
; #pragma unroll
;         for (int t = 0; t < 4; ++t) {
;             const s16x4 lo = __builtin_amdgcn_ds_read_tr16_b64_v4i16((LAS s16x4*)(vb + (16 * ks) * 256 + rd.vo[t]));
;             const s16x4 hi = __builtin_amdgcn_ds_read_tr16_b64_v4i16((LAS s16x4*)(vb + (16 * ks + 8) * 256 + rd.vo[t]));
;             const bf16x8 vf = __builtin_shufflevector(lo, hi, 0, 1, 2, 3, 4, 5, 6, 7);
;             o[t] = MFMA32(vf, pf[ks], o[t]);
;         }
; }
; template <int DQ, class Drv>
; DI void at_run3(LAS unsigned char* lds, const Drv& D, const int n, const AtRd& rd, const AtDma& dm, const bf16x8 (&qf)[DQ / 16], f32x16 (&o)[4], float& m, float& l, const float c2, const int lane, const int wave) {
;     ...
;         if (j + 2 < n) { if (DQ == 192) asm volatile("s_waitcnt vmcnt(5)" ::: "memory"); else asm volatile("s_waitcnt vmcnt(4)" ::: "memory"); }
;         else asm volatile("s_waitcnt vmcnt(0)" ::: "memory");
;         __syncthreads();
.LBB0_555:
	v_exp_f32_e32 v2, v98
	v_exp_f32_e32 v192, v82
	v_exp_f32_e32 v8, v99
	v_exp_f32_e32 v193, v83
	v_exp_f32_e32 v14, v100
	v_exp_f32_e32 v194, v84
	v_exp_f32_e32 v15, v101
	v_exp_f32_e32 v195, v85
	v_add_f32_e32 v4, v192, v2
	v_exp_f32_e32 v82, v102
	v_exp_f32_e32 v196, v86
	v_add_f32_e32 v4, 0, v4
	v_add_f32_e32 v5, v193, v8
	v_exp_f32_e32 v6, v103
	v_exp_f32_e32 v16, v87
	v_add_f32_e32 v4, v5, v4
	v_add_f32_e32 v5, v194, v14
	v_add_f32_e32 v4, v5, v4
	v_add_f32_e32 v5, v195, v15
	v_add_f32_e32 v7, v5, v4
	v_add_f32_e32 v17, v196, v82
	v_pk_add_f32 v[4:5], v[16:17], v[6:7]
	v_exp_f32_e32 v7, v104
	v_pk_add_f32 v[12:13], v[4:5], v[4:5] op_sel_hi:[0,1]
	v_exp_f32_e32 v17, v88
	v_exp_f32_e32 v12, v105
	v_exp_f32_e32 v98, v89
	v_exp_f32_e32 v197, v90
	v_add_f32_e32 v99, v17, v7
	v_exp_f32_e32 v102, v91
	v_pk_add_f32 v[4:5], v[98:99], v[12:13]
	v_exp_f32_e32 v99, v106
	v_pk_add_f32 v[100:101], v[4:5], v[4:5] op_sel_hi:[0,1]
	v_exp_f32_e32 v100, v107
	v_exp_f32_e32 v106, v93
	v_add_f32_e32 v103, v197, v99
	v_exp_f32_e32 v198, v110
	v_pk_add_f32 v[4:5], v[102:103], v[100:101]
	v_exp_f32_e32 v101, v108
	v_pk_add_f32 v[104:105], v[4:5], v[4:5] op_sel_hi:[0,1]
	v_exp_f32_e32 v103, v92
	v_exp_f32_e32 v104, v109
	v_cvt_pk_bf16_f32 v4, v2, v8
	v_lshl_add_u32 v2, s70, 14, v188
	v_add_u32_e32 v2, 0x6000, v2
	v_add_f32_e32 v107, v103, v101
	v_pk_add_f32 v[86:87], v[106:107], v[104:105]
	v_add_u32_e32 v105, v2, v183
	s_nop 0
	ds_read_b64_tr_b16 v[8:9], v105 offset:49152
	ds_read_b64_tr_b16 v[10:11], v105 offset:51200
	v_add_u32_e32 v107, v2, v184
	v_pk_add_f32 v[108:109], v[86:87], v[86:87] op_sel_hi:[0,1]
	v_exp_f32_e32 v200, v94
	v_cvt_pk_bf16_f32 v5, v14, v15
	v_cvt_pk_bf16_f32 v6, v82, v6
	v_cvt_pk_bf16_f32 v7, v7, v12
	ds_read_b64_tr_b16 v[12:13], v107 offset:49152
	ds_read_b64_tr_b16 v[14:15], v107 offset:51200
	ds_read_b64_tr_b16 v[82:83], v105 offset:53248
	ds_read_b64_tr_b16 v[84:85], v105 offset:55296
	v_exp_f32_e32 v108, v111
	v_exp_f32_e32 v94, v95
	v_add_u32_e32 v199, v2, v185
	v_add_u32_e32 v2, v2, v186
	s_waitcnt lgkmcnt(4)
	v_mfma_f32_32x32x16_bf16 v[66:81], v[8:11], v[4:7], v[66:81]
	ds_read_b64_tr_b16 v[8:9], v199 offset:49152
	ds_read_b64_tr_b16 v[10:11], v199 offset:51200
	ds_read_b64_tr_b16 v[86:87], v107 offset:53248
	ds_read_b64_tr_b16 v[88:89], v107 offset:55296
	v_add_f32_e32 v95, v200, v198
	v_pk_add_f32 v[110:111], v[94:95], v[108:109]
	v_exp_f32_e32 v95, v112
	v_pk_add_f32 v[110:111], v[110:111], v[110:111] op_sel_hi:[0,1]
	v_exp_f32_e32 v110, v113
	s_add_i32 s68, s68, 1
	s_waitcnt lgkmcnt(6)
	v_mfma_f32_32x32x16_bf16 v[50:65], v[12:15], v[4:7], v[50:65]
	ds_read_b64_tr_b16 v[12:13], v2 offset:49152
	ds_read_b64_tr_b16 v[14:15], v2 offset:51200
	ds_read_b64_tr_b16 v[90:91], v199 offset:53248
	ds_read_b64_tr_b16 v[92:93], v199 offset:55296
	s_add_i32 s69, s69, 64
	s_cmp_eq_u32 s10, s68
	s_waitcnt lgkmcnt(6)
	v_mfma_f32_32x32x16_bf16 v[34:49], v[8:11], v[4:7], v[34:49]
	ds_read_b64_tr_b16 v[8:9], v2 offset:53248
	ds_read_b64_tr_b16 v[10:11], v2 offset:55296
	s_waitcnt lgkmcnt(4)
	v_mfma_f32_32x32x16_bf16 v[18:33], v[12:15], v[4:7], v[18:33]
	v_cvt_pk_bf16_f32 v4, v99, v100
	v_cvt_pk_bf16_f32 v5, v101, v104
	v_cvt_pk_bf16_f32 v6, v198, v108
	v_cvt_pk_bf16_f32 v7, v95, v110
	s_nop 1
	v_mfma_f32_32x32x16_bf16 v[66:81], v[82:85], v[4:7], v[66:81]
	v_mfma_f32_32x32x16_bf16 v[50:65], v[86:89], v[4:7], v[50:65]
	s_waitcnt lgkmcnt(2)
	v_mfma_f32_32x32x16_bf16 v[34:49], v[90:93], v[4:7], v[34:49]
	s_waitcnt lgkmcnt(0)
	v_mfma_f32_32x32x16_bf16 v[18:33], v[8:11], v[4:7], v[18:33]
	ds_read_b64_tr_b16 v[4:5], v105 offset:57344
	ds_read_b64_tr_b16 v[6:7], v105 offset:59392
	v_cvt_pk_bf16_f32 v8, v192, v193
	v_cvt_pk_bf16_f32 v9, v194, v195
	v_cvt_pk_bf16_f32 v10, v196, v16
	v_cvt_pk_bf16_f32 v11, v17, v98
	ds_read_b64_tr_b16 v[12:13], v105 offset:61440
	ds_read_b64_tr_b16 v[14:15], v105 offset:63488
	s_waitcnt lgkmcnt(2)
	v_mfma_f32_32x32x16_bf16 v[66:81], v[4:7], v[8:11], v[66:81]
	ds_read_b64_tr_b16 v[4:5], v107 offset:57344
	ds_read_b64_tr_b16 v[6:7], v107 offset:59392
	ds_read_b64_tr_b16 v[82:83], v107 offset:61440
	ds_read_b64_tr_b16 v[84:85], v107 offset:63488
	s_waitcnt lgkmcnt(2)
	v_mfma_f32_32x32x16_bf16 v[50:65], v[4:7], v[8:11], v[50:65]
	ds_read_b64_tr_b16 v[4:5], v199 offset:57344
	ds_read_b64_tr_b16 v[6:7], v199 offset:59392
	ds_read_b64_tr_b16 v[86:87], v199 offset:61440
	ds_read_b64_tr_b16 v[88:89], v199 offset:63488
	s_waitcnt lgkmcnt(2)
	v_mfma_f32_32x32x16_bf16 v[34:49], v[4:7], v[8:11], v[34:49]
	ds_read_b64_tr_b16 v[4:5], v2 offset:57344
	ds_read_b64_tr_b16 v[6:7], v2 offset:59392
	ds_read_b64_tr_b16 v[90:91], v2 offset:61440
	ds_read_b64_tr_b16 v[92:93], v2 offset:63488
	v_exp_f32_e32 v2, v96
	s_cbranch_scc1 .Lmla_w0
	s_waitcnt vmcnt(5)
	s_branch .Lmla_wd

; #define LAS __attribute__((address_space(3)))
; #define MFMA32(a, b, c) __builtin_amdgcn_mfma_f32_32x32x16_bf16((a), (b), (c), 0, 0, 0)
;     DI const char* kb(int j) const { return KV + (size_t)keyrow0(j) * 4096 + head * 512; }
;     DI NoBias bias(int) const { return NoBias(); }
; #pragma unroll
;     for (int i = 0; i < 16; ++i) { s0[i] = init; s1[i] = init; }
;     const LAS unsigned char* kp0 = ks + rd.kbase; const LAS unsigned char* kp1 = ks + rd.kbase1;
; #pragma unroll
;     for (int s = 0; s < DQ / 16; ++s) {
;         const LAS unsigned char* kp = (DQ == 128) ? ((s >> 2) ? kp1 : kp0) : kp0 + ((s >> 2) << 7);
;         const bf16x8 a0 = *(const LAS bf16x8*)(kp + rd.ko[s & 3]);
;         const bf16x8 a1 = *(const LAS bf16x8*)(kp + 32 * (DQ * 2) + rd.ko[s & 3]);
;         s0 = MFMA32(a0, qf[s], s0); s1 = MFMA32(a1, qf[s], s1);
;     }
; }
; template <class BiasFn, bool PRE = false>
; DI void at_sm(f32x16& s0, f32x16& s1, f32x16 (&o)[4], float& m, float& l, const float c2, const BiasFn& bias, const int lane, bf16x8 (&pf)[4]) {
;     const int h = lane >> 5;
;     const float nm = -m;
;     int mi = (int)0x80000000;
; #pragma unroll
;     for (int i = 0; i < 16; ++i) {
;         const int key = (i & 3) + 8 * (i >> 2) + 4 * h;
;         if (!PRE) { s0[i] = fmaf(s0[i], c2, bias(key, nm)); s1[i] = fmaf(s1[i], c2, bias(32 + key, nm)); }
;         mi = max(mi, max((int)__float_as_uint(s0[i]), (int)__float_as_uint(s1[i])));
;     }
;     { const auto sw = __builtin_amdgcn_permlane32_swap((unsigned)mi, (unsigned)mi, false, false); mi = max((int)sw[0], (int)sw[1]); }
;     const float mx = __uint_as_float((unsigned)mi);
; template <int DQ, class Drv>
; DI void at_run3(LAS unsigned char* lds, const Drv& D, const int n, const AtRd& rd, const AtDma& dm, const bf16x8 (&qf)[DQ / 16], f32x16 (&o)[4], float& m, float& l, const float c2, const int lane, const int wave) {
;     ...
;     for (int j = 0; j < n; ++j) {
;         const int nx2 = cur == 0 ? 2 : cur - 1;
;         if (j + 2 < n) { at_dma_k<DQ>(lds + nx2 * AT4_SLOT, D.kb(j + 2), D.rb(j + 2), dm, wave); at_dma_v(lds + nx2 * AT4_SLOT + AT_KSLOT, D.vb(j + 2), dm, wave); }
;         if (D.act(j)) {
;             f32x16 a0, a1;
;             at_qk<DQ>(lds + cur * AT4_SLOT, rd, qf, a0, a1);
;             at_sm_pv(lds + cur * AT4_SLOT + AT_KSLOT, rd, a0, a1, o, m, l, c2, D.bias(j), lane);
;         }
.Lmla_wd:
	s_waitcnt lgkmcnt(0)
	s_barrier
	v_mfma_f32_32x32x16_bf16 v[18:33], v[4:7], v[8:11], v[18:33]
	v_exp_f32_e32 v8, v97
	v_cvt_pk_bf16_f32 v4, v197, v102
	v_cvt_pk_bf16_f32 v5, v103, v106
	v_cvt_pk_bf16_f32 v6, v200, v94
	v_cvt_pk_bf16_f32 v7, v2, v8
	v_add_f32_e32 v9, v2, v95
	v_pk_add_f32 v[8:9], v[8:9], v[110:111]
	v_mfma_f32_32x32x16_bf16 v[66:81], v[12:15], v[4:7], v[66:81]
	v_add_f32_e32 v2, v8, v9
	v_add_f32_e32 v173, v173, v2
	v_mfma_f32_32x32x16_bf16 v[50:65], v[82:85], v[4:7], v[50:65]
	v_mfma_f32_32x32x16_bf16 v[34:49], v[86:89], v[4:7], v[34:49]
	v_mfma_f32_32x32x16_bf16 v[18:33], v[90:93], v[4:7], v[18:33]
	s_cbranch_scc1 .LBB0_558
.LBB0_556:
	s_mov_b32 s70, s98
	s_mov_b32 s71, s99
	s_add_i32 s98, s98, 1
	s_cmp_eq_u32 s98, 3
	s_cselect_b32 s98, 0, s98
	s_add_i32 s99, s99, 1
	s_cmp_eq_u32 s99, 3
	s_cselect_b32 s99, 0, s99
	s_add_i32 s100, s68, 2
	s_cmp_gt_u32 s100, s10
	s_cbranch_scc1 .Lmla_nodma
	s_add_i32 s100, s69, 64
	s_cmp_lt_u32 s68, 2
	s_cselect_b64 vcc, -1, 0
	v_cndmask_b32_e32 v2, v175, v178, vcc
	v_add_u32_e32 v4, s100, v2
	v_ashrrev_i32_e32 v5, 31, v4
	v_lshlrev_b64 v[6:7], 12, v[4:5]
	v_lshlrev_b64 v[4:5], 7, v[4:5]
	s_mul_i32 s72, s71, 0x6000
	v_lshl_add_u64 v[6:7], s[30:31], 0, v[6:7]
	v_lshl_add_u64 v[4:5], s[14:15], 0, v[4:5]
	s_add_i32 s72, s27, s72
	v_cndmask_b32_e64 v9, v5, v7, s[2:3]
	v_cndmask_b32_e64 v8, v4, v6, s[2:3]
	v_lshl_add_u64 v[8:9], v[8:9], 0, v[162:163]
	s_mov_b32 m0, s72
	s_lshl_b32 s71, s71, 14
	global_load_lds_dwordx4 v[8:9], off
	v_cndmask_b32_e64 v9, v5, v7, s[4:5]
	v_cndmask_b32_e64 v8, v4, v6, s[4:5]
	v_lshl_add_u64 v[8:9], v[8:9], 0, v[164:165]
	s_add_i32 m0, s72, 0x2000
	v_cndmask_b32_e64 v5, v5, v7, s[6:7]
	v_cndmask_b32_e64 v4, v4, v6, s[6:7]
	global_load_lds_dwordx4 v[8:9], off
	v_lshl_add_u64 v[4:5], v[4:5], 0, v[166:167]
	s_add_i32 m0, s72, 0x4000
	s_add_i32 s71, s27, s71
	global_load_lds_dwordx4 v[4:5], off
	v_lshl_add_u64 v[4:5], v[6:7], 0, v[168:169]
	s_add_i32 m0, s71, 0x12000
	v_lshl_add_u64 v[4:5], v[4:5], 0, s[18:19]
	global_load_lds_dwordx4 v[4:5], off
	v_lshl_add_u64 v[4:5], v[6:7], 0, v[170:171]
	s_add_i32 m0, s71, 0x14000
	v_lshl_add_u64 v[4:5], v[4:5], 0, s[18:19]
	global_load_lds_dwordx4 v[4:5], off
.Lmla_nodma:
	s_mul_i32 s71, s70, 0x6000
	v_add_u32_e32 v2, s71, v187
	v_add_u32_e32 v16, v2, v1
	ds_read_b128 v[4:7], v16
	ds_read_b128 v[8:11], v16 offset:128
	v_xor_b32_e32 v82, 0x80000000, v179
	v_mov_b32_e32 v83, v82
	v_mov_b32_e32 v84, v82
	v_mov_b32_e32 v85, v82
	v_mov_b32_e32 v86, v82
	v_mov_b32_e32 v87, v82
	v_mov_b32_e32 v88, v82
	v_mov_b32_e32 v89, v82
	v_mov_b32_e32 v90, v82
	v_mov_b32_e32 v91, v82
	v_mov_b32_e32 v92, v82
	v_mov_b32_e32 v93, v82
	v_mov_b32_e32 v94, v82
	v_mov_b32_e32 v95, v82
	v_mov_b32_e32 v96, v82
	v_mov_b32_e32 v97, v82
	v_add_u32_e32 v17, v2, v180
	v_add_u32_e32 v216, v2, v181
	s_waitcnt lgkmcnt(0)
	v_mfma_f32_32x32x16_bf16 v[98:113], v[4:7], v[158:161], v[82:97]
	ds_read_b128 v[4:7], v16 offset:12288
	ds_read_b128 v[12:15], v16 offset:256
	v_add_u32_e32 v2, v2, v182
	s_waitcnt lgkmcnt(0)
	v_mfma_f32_32x32x16_bf16 v[82:97], v[4:7], v[158:161], v[82:97]
	ds_read_b128 v[4:7], v17
	ds_read_b128 v[192:195], v17 offset:128
	s_waitcnt lgkmcnt(0)
	v_mfma_f32_32x32x16_bf16 v[98:113], v[4:7], v[154:157], v[98:113]
	ds_read_b128 v[4:7], v17 offset:12288
	ds_read_b128 v[196:199], v17 offset:256
	s_waitcnt lgkmcnt(0)
	v_mfma_f32_32x32x16_bf16 v[82:97], v[4:7], v[154:157], v[82:97]
	ds_read_b128 v[4:7], v216
	ds_read_b128 v[200:203], v216 offset:128
	s_waitcnt lgkmcnt(0)
	v_mfma_f32_32x32x16_bf16 v[98:113], v[4:7], v[150:153], v[98:113]
	ds_read_b128 v[4:7], v216 offset:12288
	ds_read_b128 v[204:207], v216 offset:256
	s_waitcnt lgkmcnt(0)
	v_mfma_f32_32x32x16_bf16 v[82:97], v[4:7], v[150:153], v[82:97]
	ds_read_b128 v[4:7], v2
	ds_read_b128 v[208:211], v2 offset:128
	s_waitcnt lgkmcnt(0)
	v_mfma_f32_32x32x16_bf16 v[98:113], v[4:7], v[146:149], v[98:113]
	ds_read_b128 v[4:7], v2 offset:12288
	ds_read_b128 v[212:215], v2 offset:256
	s_waitcnt lgkmcnt(0)
	v_mfma_f32_32x32x16_bf16 v[82:97], v[4:7], v[146:149], v[82:97]
	v_mfma_f32_32x32x16_bf16 v[98:113], v[8:11], v[142:145], v[98:113]
	ds_read_b128 v[4:7], v16 offset:12416
	ds_read_b128 v[8:11], v16 offset:12544
	s_waitcnt lgkmcnt(0)
	v_mfma_f32_32x32x16_bf16 v[82:97], v[4:7], v[142:145], v[82:97]
	v_mfma_f32_32x32x16_bf16 v[98:113], v[192:195], v[138:141], v[98:113]
	ds_read_b128 v[4:7], v17 offset:12416
	ds_read_b128 v[192:195], v17 offset:12544
	s_waitcnt lgkmcnt(0)
	v_mfma_f32_32x32x16_bf16 v[82:97], v[4:7], v[138:141], v[82:97]
	v_mfma_f32_32x32x16_bf16 v[98:113], v[200:203], v[134:137], v[98:113]
	ds_read_b128 v[4:7], v216 offset:12416
	ds_read_b128 v[200:203], v216 offset:12544
	s_waitcnt lgkmcnt(0)
	v_mfma_f32_32x32x16_bf16 v[82:97], v[4:7], v[134:137], v[82:97]
	v_mfma_f32_32x32x16_bf16 v[98:113], v[208:211], v[130:133], v[98:113]
	ds_read_b128 v[4:7], v2 offset:12416
	ds_read_b128 v[208:211], v2 offset:12544
	s_waitcnt lgkmcnt(0)
	v_mfma_f32_32x32x16_bf16 v[82:97], v[4:7], v[130:133], v[82:97]
	v_mfma_f32_32x32x16_bf16 v[98:113], v[12:15], v[126:129], v[98:113]
	v_mfma_f32_32x32x16_bf16 v[82:97], v[8:11], v[126:129], v[82:97]
	v_mfma_f32_32x32x16_bf16 v[98:113], v[196:199], v[122:125], v[98:113]
	v_mfma_f32_32x32x16_bf16 v[82:97], v[192:195], v[122:125], v[82:97]
	v_mfma_f32_32x32x16_bf16 v[98:113], v[204:207], v[118:121], v[98:113]
	v_mfma_f32_32x32x16_bf16 v[82:97], v[200:203], v[118:121], v[82:97]
	v_mfma_f32_32x32x16_bf16 v[98:113], v[212:215], v[114:117], v[98:113]
	v_mfma_f32_32x32x16_bf16 v[82:97], v[208:211], v[114:117], v[82:97]
	s_nop 11
	v_max_i32_e32 v2, v99, v83
	v_max3_i32 v2, v98, v82, v2
	v_max_i32_e32 v4, v100, v84
	v_max_i32_e32 v5, v101, v85
	v_max3_i32 v2, v2, v4, v5
	v_max_i32_e32 v4, v102, v86
	v_max_i32_e32 v5, v103, v87
	v_max3_i32 v2, v2, v4, v5
	v_max_i32_e32 v4, v104, v88
	v_max_i32_e32 v5, v105, v89
	v_max3_i32 v2, v2, v4, v5
	v_max_i32_e32 v4, v106, v90
	v_max_i32_e32 v5, v107, v91
	v_max3_i32 v2, v2, v4, v5
	v_max_i32_e32 v4, v108, v92
	v_max_i32_e32 v5, v109, v93
	v_max3_i32 v2, v2, v4, v5
	v_max_i32_e32 v4, v110, v94
	v_max_i32_e32 v5, v111, v95
	v_max3_i32 v2, v2, v4, v5
	v_max_i32_e32 v4, v112, v96
	v_max_i32_e32 v5, v113, v97
	v_max3_i32 v2, v2, v4, v5
	v_mov_b32_e32 v4, v2
	s_nop 1
	v_permlane32_swap_b32_e32 v2, v4
	v_max_i32_e32 v2, v2, v4
	v_cmp_lt_f32_e32 vcc, s58, v2
	s_cbranch_vccz .LBB0_555
; #define LAS __attribute__((address_space(3)))
; #define MFMA32(a, b, c) __builtin_amdgcn_mfma_f32_32x32x16_bf16((a), (b), (c), 0, 0, 0)
; #pragma unroll
;     for (int i = 0; i < 16; ++i) { s0[i] = init; s1[i] = init; }
;     const LAS unsigned char* kp0 = ks + rd.kbase; const LAS unsigned char* kp1 = ks + rd.kbase1;
; #pragma unroll
;     for (int s = 0; s < DQ / 16; ++s) {
;         const LAS unsigned char* kp = (DQ == 128) ? ((s >> 2) ? kp1 : kp0) : kp0 + ((s >> 2) << 7);
;         const bf16x8 a0 = *(const LAS bf16x8*)(kp + rd.ko[s & 3]);
;         const bf16x8 a1 = *(const LAS bf16x8*)(kp + 32 * (DQ * 2) + rd.ko[s & 3]);
;         s0 = MFMA32(a0, qf[s], s0); s1 = MFMA32(a1, qf[s], s1);
;     }
; }
; template <class BiasFn, bool PRE = false>
; DI void at_sm(f32x16& s0, f32x16& s1, f32x16 (&o)[4], float& m, float& l, const float c2, const BiasFn& bias, const int lane, bf16x8 (&pf)[4]) {
;     ...
;     if (__any(mx > 8.0f)) {
;         const float d = fmaxf(mx, 0.f), alpha = __builtin_amdgcn_exp2f(-d);
;         m += d; l *= alpha;
; #pragma unroll
;         for (int t = 0; t < 4; ++t)
; #pragma unroll
;             for (int i = 0; i < 16; ++i) o[t][i] *= alpha;
; #pragma unroll
;         for (int i = 0; i < 16; ++i) { s0[i] -= d; s1[i] -= d; }
;     }
	v_max_f32_e32 v2, v2, v2
	v_max_f32_e32 v4, 0, v2
	v_exp_f32_e64 v2, -v4
	v_add_f32_e32 v179, v179, v4
	v_sub_f32_e32 v113, v113, v4
	v_sub_f32_e32 v112, v112, v4
	v_mul_f32_e32 v173, v173, v2
	v_pk_mul_f32 v[80:81], v[80:81], v[2:3] op_sel_hi:[1,0]
	v_pk_mul_f32 v[78:79], v[78:79], v[2:3] op_sel_hi:[1,0]
	v_pk_mul_f32 v[76:77], v[76:77], v[2:3] op_sel_hi:[1,0]
	v_pk_mul_f32 v[74:75], v[74:75], v[2:3] op_sel_hi:[1,0]
	v_pk_mul_f32 v[72:73], v[72:73], v[2:3] op_sel_hi:[1,0]
	v_pk_mul_f32 v[70:71], v[70:71], v[2:3] op_sel_hi:[1,0]
	v_pk_mul_f32 v[68:69], v[68:69], v[2:3] op_sel_hi:[1,0]
	v_pk_mul_f32 v[66:67], v[66:67], v[2:3] op_sel_hi:[1,0]
	v_pk_mul_f32 v[64:65], v[64:65], v[2:3] op_sel_hi:[1,0]
	v_pk_mul_f32 v[62:63], v[62:63], v[2:3] op_sel_hi:[1,0]
	v_pk_mul_f32 v[60:61], v[60:61], v[2:3] op_sel_hi:[1,0]
	v_pk_mul_f32 v[58:59], v[58:59], v[2:3] op_sel_hi:[1,0]
	v_pk_mul_f32 v[56:57], v[56:57], v[2:3] op_sel_hi:[1,0]
	v_pk_mul_f32 v[54:55], v[54:55], v[2:3] op_sel_hi:[1,0]
	v_pk_mul_f32 v[52:53], v[52:53], v[2:3] op_sel_hi:[1,0]
	v_pk_mul_f32 v[50:51], v[50:51], v[2:3] op_sel_hi:[1,0]
	v_pk_mul_f32 v[48:49], v[48:49], v[2:3] op_sel_hi:[1,0]
	v_pk_mul_f32 v[46:47], v[46:47], v[2:3] op_sel_hi:[1,0]
	v_pk_mul_f32 v[44:45], v[44:45], v[2:3] op_sel_hi:[1,0]
	v_pk_mul_f32 v[42:43], v[42:43], v[2:3] op_sel_hi:[1,0]
	v_pk_mul_f32 v[40:41], v[40:41], v[2:3] op_sel_hi:[1,0]
	v_pk_mul_f32 v[38:39], v[38:39], v[2:3] op_sel_hi:[1,0]
	v_pk_mul_f32 v[36:37], v[36:37], v[2:3] op_sel_hi:[1,0]
	v_pk_mul_f32 v[34:35], v[34:35], v[2:3] op_sel_hi:[1,0]
	v_pk_mul_f32 v[32:33], v[32:33], v[2:3] op_sel_hi:[1,0]
	v_pk_mul_f32 v[30:31], v[30:31], v[2:3] op_sel_hi:[1,0]
	v_pk_mul_f32 v[28:29], v[28:29], v[2:3] op_sel_hi:[1,0]
	v_pk_mul_f32 v[26:27], v[26:27], v[2:3] op_sel_hi:[1,0]
	v_pk_mul_f32 v[24:25], v[24:25], v[2:3] op_sel_hi:[1,0]
	v_pk_mul_f32 v[22:23], v[22:23], v[2:3] op_sel_hi:[1,0]
	v_pk_mul_f32 v[20:21], v[20:21], v[2:3] op_sel_hi:[1,0]
	v_pk_mul_f32 v[18:19], v[18:19], v[2:3] op_sel_hi:[1,0]
	v_sub_f32_e32 v111, v111, v4
	v_sub_f32_e32 v110, v110, v4
	v_sub_f32_e32 v109, v109, v4
	v_sub_f32_e32 v108, v108, v4
	v_sub_f32_e32 v107, v107, v4
	v_sub_f32_e32 v106, v106, v4
	v_sub_f32_e32 v105, v105, v4
	v_sub_f32_e32 v104, v104, v4
	v_sub_f32_e32 v103, v103, v4
	v_sub_f32_e32 v102, v102, v4
	v_sub_f32_e32 v101, v101, v4
	v_sub_f32_e32 v100, v100, v4
	v_sub_f32_e32 v99, v99, v4
	v_sub_f32_e32 v98, v98, v4
	v_sub_f32_e32 v97, v97, v4
	v_sub_f32_e32 v96, v96, v4
	v_sub_f32_e32 v95, v95, v4
	v_sub_f32_e32 v94, v94, v4
	v_sub_f32_e32 v93, v93, v4
	v_sub_f32_e32 v92, v92, v4
	v_sub_f32_e32 v91, v91, v4
	v_sub_f32_e32 v90, v90, v4
	v_sub_f32_e32 v89, v89, v4
	v_sub_f32_e32 v88, v88, v4
	v_sub_f32_e32 v87, v87, v4
	v_sub_f32_e32 v86, v86, v4
	v_sub_f32_e32 v85, v85, v4
	v_sub_f32_e32 v84, v84, v4
	v_sub_f32_e32 v83, v83, v4
	v_sub_f32_e32 v82, v82, v4
	s_branch .LBB0_555
.LBB0_558:
	s_mov_b32 s10, s98
	s_mul_i32 s30, s10, 0x6000
	v_add_u32_e32 v2, s30, v187
	v_add_u32_e32 v16, v2, v1
	ds_read_b128 v[4:7], v16
	ds_read_b128 v[8:11], v16 offset:128
	v_xor_b32_e32 v82, 0x80000000, v179
	v_mov_b32_e32 v83, v82
	v_mov_b32_e32 v84, v82
	v_mov_b32_e32 v85, v82
	v_mov_b32_e32 v86, v82
	v_mov_b32_e32 v87, v82
	v_mov_b32_e32 v88, v82
	v_mov_b32_e32 v89, v82
	v_mov_b32_e32 v90, v82
	v_mov_b32_e32 v91, v82
	v_mov_b32_e32 v92, v82
	v_mov_b32_e32 v93, v82
	v_mov_b32_e32 v94, v82
	v_mov_b32_e32 v95, v82
	v_mov_b32_e32 v96, v82
	v_mov_b32_e32 v97, v82
	v_add_u32_e32 v17, v2, v180
	v_add_u32_e32 v175, v2, v181
	s_waitcnt lgkmcnt(1)
	v_mfma_f32_32x32x16_bf16 v[98:113], v[4:7], v[158:161], v[82:97]
	ds_read_b128 v[4:7], v16 offset:12288
	ds_read_b128 v[12:15], v16 offset:256
	v_add_u32_e32 v2, v2, v182
	s_waitcnt lgkmcnt(1)
	v_mfma_f32_32x32x16_bf16 v[82:97], v[4:7], v[158:161], v[82:97]
	ds_read_b128 v[4:7], v17
	ds_read_b128 v[158:161], v17 offset:128
	s_waitcnt lgkmcnt(1)
	v_mfma_f32_32x32x16_bf16 v[98:113], v[4:7], v[154:157], v[98:113]
	ds_read_b128 v[4:7], v17 offset:12288
	ds_read_b128 v[192:195], v17 offset:256
	s_waitcnt lgkmcnt(1)
	v_mfma_f32_32x32x16_bf16 v[82:97], v[4:7], v[154:157], v[82:97]
	ds_read_b128 v[4:7], v175
	ds_read_b128 v[154:157], v175 offset:128
	s_waitcnt lgkmcnt(1)
	v_mfma_f32_32x32x16_bf16 v[98:113], v[4:7], v[150:153], v[98:113]
	ds_read_b128 v[4:7], v175 offset:12288
	ds_read_b128 v[196:199], v175 offset:256
	s_waitcnt lgkmcnt(1)
	v_mfma_f32_32x32x16_bf16 v[82:97], v[4:7], v[150:153], v[82:97]
	ds_read_b128 v[4:7], v2
	ds_read_b128 v[150:153], v2 offset:128
	s_waitcnt lgkmcnt(1)
	v_mfma_f32_32x32x16_bf16 v[98:113], v[4:7], v[146:149], v[98:113]
	ds_read_b128 v[4:7], v2 offset:12288
	ds_read_b128 v[200:203], v2 offset:256
	s_waitcnt lgkmcnt(1)
	v_mfma_f32_32x32x16_bf16 v[82:97], v[4:7], v[146:149], v[82:97]
	v_mfma_f32_32x32x16_bf16 v[98:113], v[8:11], v[142:145], v[98:113]
	ds_read_b128 v[4:7], v16 offset:12416
	ds_read_b128 v[8:11], v16 offset:12544
	s_waitcnt lgkmcnt(1)
; #define LAS __attribute__((address_space(3)))
; #define MFMA32(a, b, c) __builtin_amdgcn_mfma_f32_32x32x16_bf16((a), (b), (c), 0, 0, 0)
;     DI NoBias bias(int) const { return NoBias(); }
;     DI WinBias bias(int q) const { const int j = tid_(q); WinBias B; B.base = j < 4 ? 100 : qpos - (k0base + 64 * (j - 4)) + 128; return B; }
;     ...
;     for (int s = 0; s < DQ / 16; ++s) {
;         const LAS unsigned char* kp = (DQ == 128) ? ((s >> 2) ? kp1 : kp0) : kp0 + ((s >> 2) << 7);
;         const bf16x8 a0 = *(const LAS bf16x8*)(kp + rd.ko[s & 3]);
;         const bf16x8 a1 = *(const LAS bf16x8*)(kp + 32 * (DQ * 2) + rd.ko[s & 3]);
;         s0 = MFMA32(a0, qf[s], s0); s1 = MFMA32(a1, qf[s], s1);
;     }
; }
; template <class BiasFn, bool PRE = false>
; DI void at_sm(f32x16& s0, f32x16& s1, f32x16 (&o)[4], float& m, float& l, const float c2, const BiasFn& bias, const int lane, bf16x8 (&pf)[4]) {
;     const int h = lane >> 5;
;     const float nm = -m;
;     int mi = (int)0x80000000;
; #pragma unroll
;     for (int i = 0; i < 16; ++i) {
;         const int key = (i & 3) + 8 * (i >> 2) + 4 * h;
;         if (!PRE) { s0[i] = fmaf(s0[i], c2, bias(key, nm)); s1[i] = fmaf(s1[i], c2, bias(32 + key, nm)); }
;         mi = max(mi, max((int)__float_as_uint(s0[i]), (int)__float_as_uint(s1[i])));
;     }
;     { const auto sw = __builtin_amdgcn_permlane32_swap((unsigned)mi, (unsigned)mi, false, false); mi = max((int)sw[0], (int)sw[1]); }
;     const float mx = __uint_as_float((unsigned)mi);
;     if (__any(mx > 8.0f)) {
;         const float d = fmaxf(mx, 0.f), alpha = __builtin_amdgcn_exp2f(-d);
;         m += d; l *= alpha;
; #pragma unroll
;         for (int t = 0; t < 4; ++t)
; #pragma unroll
;             for (int i = 0; i < 16; ++i) o[t][i] *= alpha;
; #pragma unroll
;         for (int i = 0; i < 16; ++i) { s0[i] -= d; s1[i] -= d; }
;     }
	v_mfma_f32_32x32x16_bf16 v[82:97], v[4:7], v[142:145], v[82:97]
	ds_read_b128 v[4:7], v17 offset:12416
	ds_read_b128 v[142:145], v17 offset:12544
	v_mfma_f32_32x32x16_bf16 v[98:113], v[158:161], v[138:141], v[98:113]
	s_waitcnt lgkmcnt(1)
	v_mfma_f32_32x32x16_bf16 v[82:97], v[4:7], v[138:141], v[82:97]
	ds_read_b128 v[4:7], v175 offset:12416
	ds_read_b128 v[138:141], v175 offset:12544
	v_mfma_f32_32x32x16_bf16 v[98:113], v[154:157], v[134:137], v[98:113]
	s_waitcnt lgkmcnt(1)
	v_mfma_f32_32x32x16_bf16 v[82:97], v[4:7], v[134:137], v[82:97]
	ds_read_b128 v[4:7], v2 offset:12416
	ds_read_b128 v[134:137], v2 offset:12544
	v_mfma_f32_32x32x16_bf16 v[98:113], v[150:153], v[130:133], v[98:113]
	s_waitcnt lgkmcnt(1)
	v_mfma_f32_32x32x16_bf16 v[82:97], v[4:7], v[130:133], v[82:97]
	v_mfma_f32_32x32x16_bf16 v[98:113], v[12:15], v[126:129], v[98:113]
	v_mfma_f32_32x32x16_bf16 v[82:97], v[8:11], v[126:129], v[82:97]
	v_mfma_f32_32x32x16_bf16 v[98:113], v[192:195], v[122:125], v[98:113]
	v_mfma_f32_32x32x16_bf16 v[82:97], v[142:145], v[122:125], v[82:97]
	v_mfma_f32_32x32x16_bf16 v[98:113], v[196:199], v[118:121], v[98:113]
	v_mfma_f32_32x32x16_bf16 v[82:97], v[138:141], v[118:121], v[82:97]
	v_mfma_f32_32x32x16_bf16 v[98:113], v[200:203], v[114:117], v[98:113]
	s_waitcnt lgkmcnt(0)
	v_mfma_f32_32x32x16_bf16 v[82:97], v[134:137], v[114:117], v[82:97]
	s_nop 11
	v_max_i32_e32 v2, v99, v83
	v_max3_i32 v2, v98, v82, v2
	v_max_i32_e32 v4, v100, v84
	v_max_i32_e32 v5, v101, v85
	v_max3_i32 v2, v2, v4, v5
	v_max_i32_e32 v4, v102, v86
	v_max_i32_e32 v5, v103, v87
	v_max3_i32 v2, v2, v4, v5
	v_max_i32_e32 v4, v104, v88
	v_max_i32_e32 v5, v105, v89
	v_max3_i32 v2, v2, v4, v5
	v_max_i32_e32 v4, v106, v90
	v_max_i32_e32 v5, v107, v91
	v_max3_i32 v2, v2, v4, v5
	v_max_i32_e32 v4, v108, v92
	v_max_i32_e32 v5, v109, v93
	v_max3_i32 v2, v2, v4, v5
	v_max_i32_e32 v4, v110, v94
	v_max_i32_e32 v5, v111, v95
	v_max3_i32 v2, v2, v4, v5
	v_max_i32_e32 v4, v112, v96
	v_max_i32_e32 v5, v113, v97
	v_max3_i32 v2, v2, v4, v5
	v_mov_b32_e32 v4, v2
	s_nop 1
	v_permlane32_swap_b32_e32 v2, v4
	v_max_i32_e32 v2, v2, v4
	v_cmp_lt_f32_e32 vcc, s58, v2
	s_cbranch_vccz .LBB0_549
	v_max_f32_e32 v2, v2, v2
	v_max_f32_e32 v4, 0, v2
	v_exp_f32_e64 v2, -v4
	v_sub_f32_e32 v113, v113, v4
	v_sub_f32_e32 v112, v112, v4
	v_sub_f32_e32 v111, v111, v4
	v_mul_f32_e32 v173, v173, v2
	v_pk_mul_f32 v[80:81], v[80:81], v[2:3] op_sel_hi:[1,0]
	v_pk_mul_f32 v[78:79], v[78:79], v[2:3] op_sel_hi:[1,0]
	v_pk_mul_f32 v[76:77], v[76:77], v[2:3] op_sel_hi:[1,0]
	v_pk_mul_f32 v[74:75], v[74:75], v[2:3] op_sel_hi:[1,0]
	v_pk_mul_f32 v[72:73], v[72:73], v[2:3] op_sel_hi:[1,0]
	v_pk_mul_f32 v[70:71], v[70:71], v[2:3] op_sel_hi:[1,0]
	v_pk_mul_f32 v[68:69], v[68:69], v[2:3] op_sel_hi:[1,0]
	v_pk_mul_f32 v[66:67], v[66:67], v[2:3] op_sel_hi:[1,0]
	v_pk_mul_f32 v[64:65], v[64:65], v[2:3] op_sel_hi:[1,0]
	v_pk_mul_f32 v[62:63], v[62:63], v[2:3] op_sel_hi:[1,0]
	v_pk_mul_f32 v[60:61], v[60:61], v[2:3] op_sel_hi:[1,0]
	v_pk_mul_f32 v[58:59], v[58:59], v[2:3] op_sel_hi:[1,0]
	v_pk_mul_f32 v[56:57], v[56:57], v[2:3] op_sel_hi:[1,0]
	v_pk_mul_f32 v[54:55], v[54:55], v[2:3] op_sel_hi:[1,0]
	v_pk_mul_f32 v[52:53], v[52:53], v[2:3] op_sel_hi:[1,0]
	v_pk_mul_f32 v[50:51], v[50:51], v[2:3] op_sel_hi:[1,0]
	v_pk_mul_f32 v[48:49], v[48:49], v[2:3] op_sel_hi:[1,0]
	v_pk_mul_f32 v[46:47], v[46:47], v[2:3] op_sel_hi:[1,0]
	v_pk_mul_f32 v[44:45], v[44:45], v[2:3] op_sel_hi:[1,0]
	v_pk_mul_f32 v[42:43], v[42:43], v[2:3] op_sel_hi:[1,0]
	v_pk_mul_f32 v[40:41], v[40:41], v[2:3] op_sel_hi:[1,0]
	v_pk_mul_f32 v[38:39], v[38:39], v[2:3] op_sel_hi:[1,0]
	v_pk_mul_f32 v[36:37], v[36:37], v[2:3] op_sel_hi:[1,0]
	v_pk_mul_f32 v[34:35], v[34:35], v[2:3] op_sel_hi:[1,0]
	v_pk_mul_f32 v[32:33], v[32:33], v[2:3] op_sel_hi:[1,0]
	v_pk_mul_f32 v[30:31], v[30:31], v[2:3] op_sel_hi:[1,0]
	v_pk_mul_f32 v[28:29], v[28:29], v[2:3] op_sel_hi:[1,0]
	v_pk_mul_f32 v[26:27], v[26:27], v[2:3] op_sel_hi:[1,0]
	v_pk_mul_f32 v[24:25], v[24:25], v[2:3] op_sel_hi:[1,0]
	v_pk_mul_f32 v[22:23], v[22:23], v[2:3] op_sel_hi:[1,0]
	v_pk_mul_f32 v[20:21], v[20:21], v[2:3] op_sel_hi:[1,0]
	v_pk_mul_f32 v[18:19], v[18:19], v[2:3] op_sel_hi:[1,0]
	v_sub_f32_e32 v110, v110, v4
	v_sub_f32_e32 v109, v109, v4
	v_sub_f32_e32 v108, v108, v4
	v_sub_f32_e32 v107, v107, v4
	v_sub_f32_e32 v106, v106, v4
	v_sub_f32_e32 v105, v105, v4
	v_sub_f32_e32 v104, v104, v4
	v_sub_f32_e32 v103, v103, v4
	v_sub_f32_e32 v102, v102, v4
	v_sub_f32_e32 v101, v101, v4
	v_sub_f32_e32 v100, v100, v4
	v_sub_f32_e32 v99, v99, v4
	v_sub_f32_e32 v98, v98, v4
	v_sub_f32_e32 v97, v97, v4
	v_sub_f32_e32 v96, v96, v4
	v_sub_f32_e32 v95, v95, v4
	v_sub_f32_e32 v94, v94, v4
	v_sub_f32_e32 v93, v93, v4
	v_sub_f32_e32 v92, v92, v4
	v_sub_f32_e32 v91, v91, v4
	v_sub_f32_e32 v90, v90, v4
	v_sub_f32_e32 v89, v89, v4
	v_sub_f32_e32 v88, v88, v4
	v_sub_f32_e32 v87, v87, v4
	v_sub_f32_e32 v86, v86, v4
	v_sub_f32_e32 v85, v85, v4
	v_sub_f32_e32 v84, v84, v4
	v_sub_f32_e32 v83, v83, v4
	v_sub_f32_e32 v82, v82, v4
	s_branch .LBB0_549
